# v133 + HGRN2 gate-mode epilogue prefix product: mov 1.0 / mov_dpp / mul triples fused into in-place v_mul_f32_dpp (209 steps, bit-identical)
# baseline (speedup 1.0000x reference)
; #define PG8_DPP_SHR(v, n) __builtin_bit_cast(float, __builtin_amdgcn_update_dpp(0x3f800000, __builtin_bit_cast(int, v), 0x110 + (n), 0xf, 0xf, false))
; __device__ __forceinline__ float bcast15(float x, int lane) { (void)lane; return __builtin_bit_cast(float, __builtin_amdgcn_update_dpp(0, __builtin_bit_cast(int, x), 0x15F, 0xf, 0xf, false)); }
; __device__ __forceinline__ float sigm_f(float x) { return __builtin_amdgcn_rcpf(1.0f + __builtin_amdgcn_exp2f(-1.4426950408889634f * x)); }
; __device__ __forceinline__ float scan16_mul(float x) {
;     ...
;     x *= PG8_DPP_SHR(x, 1); x *= PG8_DPP_SHR(x, 2); x *= PG8_DPP_SHR(x, 4); x *= PG8_DPP_SHR(x, 8);
;     ...
;     return x;
; }
;     __device__ __forceinline__ void operator()(const f32x4 (&acc)[2][2][4][2], const Unit& u, int wr, int wc, int fr, int fq) const {
;     ...
;                     for (int c = 0; c < 8; ++c) {
;                         const float z0 = acc[ai][1][2 * mp][c >> 2][c & 3], z1 = acc[ai][1][2 * mp + 1][c >> 2][c & 3];
;                         const float q0 = acc[ai][0][2 * mp][c >> 2][c & 3], q1 = acc[ai][0][2 * mp + 1][c >> 2][c & 3];
;                         const float s0 = sigm_f(z0), s1 = sigm_f(z1), om = 1.0f - lb[c];
;                         const float e0 = scan16_mul(lb[c] + om * s0);
;                         const float e1 = scan16_mul(lb[c] + om * s1) * bcast15(e0, lane);
;                         const float tt = bcast15(e1, lane);
;                         const float k0 = om * (1.0f - s0) * __builtin_amdgcn_rcpf(e0), k1 = om * (1.0f - s1) * __builtin_amdgcn_rcpf(e1);
;                         qd0[c] = q0 * e0; ki0[c] = k0; ke0[c] = k0 * tt; qd1[c] = q1 * e1; ki1[c] = k1; ke1[c] = k1 * tt; tot[c] = tt;
;                     }
.LBB0_405:
	s_nop 0
	v_lshl_or_b32 v130, s3, 7, v144
	v_ashrrev_i32_e32 v131, 31, v130
	v_lshl_add_u64 v[134:135], v[130:131], 2, s[36:37]
	global_load_dwordx4 v[130:133], v[134:135], off offset:16
	s_nop 0
	global_load_dwordx4 v[134:137], v[134:135], off
	v_lshlrev_b32_e32 v0, 7, v150
	v_and_b32_e32 v151, 0x7e780, v0
	v_mul_f32_e32 v0, 0xbfb8aa3b, v126
	v_exp_f32_e32 v0, v0
	v_mul_f32_e32 v110, 0xbfb8aa3b, v110
	v_exp_f32_e32 v110, v110
	v_add_f32_e32 v0, 1.0, v0
	v_rcp_f32_e32 v140, v0
	v_mul_f32_e32 v0, 0xbfb8aa3b, v122
	v_exp_f32_e32 v0, v0
	v_add_f32_e32 v110, 1.0, v110
	v_mul_f32_e32 v106, 0xbfb8aa3b, v106
	v_rcp_f32_e32 v182, v110
	v_add_f32_e32 v0, 1.0, v0
	v_rcp_f32_e32 v0, v0
	v_exp_f32_e32 v106, v106
	s_ashr_i32 s0, s16, 8
	s_and_b32 s0, s0, -16
	s_add_i32 s0, s0, s3
	v_add_f32_e32 v106, 1.0, v106
	v_rcp_f32_e32 v110, v106
	s_ashr_i32 s1, s0, 31
	s_lshl_b64 s[12:13], s[0:1], 19
	v_or_b32_e32 v152, s12, v144
	s_lshr_b32 s2, s16, 5
	v_mov_b32_e32 v153, s13
	s_and_b32 s2, s2, 0x7e
	s_lshl_b64 s[0:1], s[0:1], 16
	s_waitcnt vmcnt(1)
	v_mov_b32_e32 v183, v130
	s_waitcnt vmcnt(0)
	v_mov_b32_e32 v141, v134
	v_pk_add_f32 v[138:139], v[140:141], 1.0 op_sel_hi:[1,0] neg_lo:[1,0] neg_hi:[1,0]
	s_nop 0
	v_fma_f32 v122, v140, v139, v134
	v_mul_f32_e32 v138, v138, v139
	s_nop 0
	v_mul_f32_dpp v122, v122, v122 row_shr:1 row_mask:0xf bank_mask:0xf
	s_nop 1
	v_mul_f32_dpp v122, v122, v122 row_shr:2 row_mask:0xf bank_mask:0xf
	s_nop 1
	v_mul_f32_dpp v122, v122, v122 row_shr:4 row_mask:0xf bank_mask:0xf
	v_mov_b32_e32 v126, 1.0
	s_nop 1
	v_mov_b32_dpp v126, v122 row_shr:8 row_mask:0xf bank_mask:0xf
	v_mul_f32_e32 v126, v122, v126
	v_fma_f32 v122, v0, v139, v134
	v_rcp_f32_e32 v141, v126
	v_sub_f32_e32 v0, 1.0, v0
	v_mul_f32_dpp v122, v122, v122 row_shr:1 row_mask:0xf bank_mask:0xf
	v_mul_f32_e32 v164, v138, v141
	v_mul_f32_e32 v0, v0, v139
	v_mul_f32_dpp v122, v122, v122 row_shr:2 row_mask:0xf bank_mask:0xf
	v_mov_b32_e32 v141, v135
	v_mul_f32_e32 v165, v118, v126
	v_mul_f32_dpp v122, v122, v122 row_shr:4 row_mask:0xf bank_mask:0xf
	v_mov_b32_e32 v140, 1.0
	s_nop 1
	v_mov_b32_dpp v140, v122 row_shr:8 row_mask:0xf bank_mask:0xf
	v_mul_f32_e32 v122, v122, v140
	s_nop 1
	v_mul_f32_dpp v140, v126, v122 row_newbcast:15 row_mask:0xf bank_mask:0xf bound_ctrl:1
	v_rcp_f32_e32 v138, v140
	v_mov_b32_e32 v122, 0
	v_mul_f32_e32 v0, v0, v138
	v_mul_f32_e32 v138, v114, v140
	v_mul_f32_e32 v114, 0xbfb8aa3b, v127
	v_exp_f32_e32 v114, v114
	v_mov_b32_dpp v122, v140 row_newbcast:15 row_mask:0xf bank_mask:0xf
	v_mul_f32_e32 v173, v164, v122
	v_mul_f32_e32 v172, v0, v122
	v_add_f32_e32 v114, 1.0, v114
	v_rcp_f32_e32 v140, v114
	v_mul_f32_e32 v114, 0xbfb8aa3b, v123
	v_exp_f32_e32 v114, v114
	v_pk_add_f32 v[126:127], v[140:141], 1.0 op_sel_hi:[1,0] neg_lo:[1,0] neg_hi:[1,0]
	v_add_f32_e32 v114, 1.0, v114
	v_fma_f32 v118, v140, v127, v135
	v_rcp_f32_e32 v114, v114
	s_nop 0
	v_mul_f32_dpp v118, v118, v118 row_shr:1 row_mask:0xf bank_mask:0xf
	v_mul_f32_e32 v126, v126, v127
	s_nop 0
	v_mul_f32_dpp v118, v118, v118 row_shr:2 row_mask:0xf bank_mask:0xf
	s_nop 1
	v_mul_f32_dpp v118, v118, v118 row_shr:4 row_mask:0xf bank_mask:0xf
	s_nop 1
	v_mul_f32_dpp v118, v118, v118 row_shr:8 row_mask:0xf bank_mask:0xf
	v_fma_f32 v123, v114, v127, v135
	v_rcp_f32_e32 v141, v118
	v_sub_f32_e32 v114, 1.0, v114
	v_mul_f32_dpp v123, v123, v123 row_shr:1 row_mask:0xf bank_mask:0xf
	v_mul_f32_e32 v174, v126, v141
	v_mul_f32_e32 v114, v114, v127
	v_mul_f32_dpp v123, v123, v123 row_shr:2 row_mask:0xf bank_mask:0xf
	v_mul_f32_e32 v178, v119, v118
	s_nop 0
	v_mul_f32_dpp v123, v123, v123 row_shr:4 row_mask:0xf bank_mask:0xf
	v_mov_b32_e32 v140, 1.0
	s_nop 1
	v_mov_b32_dpp v140, v123 row_shr:8 row_mask:0xf bank_mask:0xf
	v_mul_f32_e32 v123, v123, v140
	s_nop 1
	v_mul_f32_dpp v140, v118, v123 row_newbcast:15 row_mask:0xf bank_mask:0xf bound_ctrl:1
	v_rcp_f32_e32 v126, v140
	v_mul_f32_e32 v176, v115, v140
	v_mul_f32_e32 v115, 0xbfb8aa3b, v124
	v_exp_f32_e32 v115, v115
	v_mul_f32_e32 v175, v114, v126
	v_mul_f32_e32 v114, 0xbfb8aa3b, v128
	v_exp_f32_e32 v114, v114
	v_add_f32_e32 v115, 1.0, v115
	v_mov_b32_e32 v123, 0
	v_rcp_f32_e32 v118, v115
	v_add_f32_e32 v114, 1.0, v114
	v_rcp_f32_e32 v114, v114
	v_mov_b32_e32 v115, v136
	v_mov_b32_dpp v123, v140 row_newbcast:15 row_mask:0xf bank_mask:0xf
	v_mov_b32_e32 v124, 0
	v_pk_add_f32 v[140:141], v[114:115], 1.0 op_sel_hi:[1,0] neg_lo:[1,0] neg_hi:[1,0]
	v_fma_f32 v114, v114, v141, v136
	v_mul_f32_e32 v177, v174, v123
	v_mul_f32_e32 v126, v175, v123
	v_mul_f32_dpp v114, v114, v114 row_shr:1 row_mask:0xf bank_mask:0xf
	s_nop 1
	v_mul_f32_dpp v114, v114, v114 row_shr:2 row_mask:0xf bank_mask:0xf
	s_nop 1
	v_mul_f32_dpp v114, v114, v114 row_shr:4 row_mask:0xf bank_mask:0xf
	s_nop 1
	v_mul_f32_dpp v114, v114, v114 row_shr:8 row_mask:0xf bank_mask:0xf
	v_fma_f32 v115, v118, v141, v136
	v_rcp_f32_e32 v128, v114
	v_mul_f32_e32 v120, v120, v114
	v_mul_f32_dpp v115, v115, v115 row_shr:1 row_mask:0xf bank_mask:0xf
	v_sub_f32_e32 v118, 1.0, v118
	v_mul_f32_e32 v118, v118, v141
	v_mul_f32_dpp v115, v115, v115 row_shr:2 row_mask:0xf bank_mask:0xf
	s_nop 1
	v_mul_f32_dpp v115, v115, v115 row_shr:4 row_mask:0xf bank_mask:0xf
	s_nop 1
	v_mul_f32_dpp v115, v115, v115 row_shr:8 row_mask:0xf bank_mask:0xf
	v_mul_f32_e32 v119, v140, v141
	v_mul_f32_e32 v128, v119, v128
	v_mul_f32_dpp v115, v114, v115 row_newbcast:15 row_mask:0xf bank_mask:0xf bound_ctrl:1
	v_mul_f32_e32 v114, 0xbfb8aa3b, v129
	v_exp_f32_e32 v114, v114
	v_mov_b32_dpp v124, v115 row_newbcast:15 row_mask:0xf bank_mask:0xf
	v_rcp_f32_e32 v119, v115
	v_mul_f32_e32 v116, v116, v115
	v_mul_f32_e32 v115, 0xbfb8aa3b, v125
; #define PG8_DPP_SHR(v, n) __builtin_bit_cast(float, __builtin_amdgcn_update_dpp(0x3f800000, __builtin_bit_cast(int, v), 0x110 + (n), 0xf, 0xf, false))
; __device__ __forceinline__ float bcast15(float x, int lane) { (void)lane; return __builtin_bit_cast(float, __builtin_amdgcn_update_dpp(0, __builtin_bit_cast(int, x), 0x15F, 0xf, 0xf, false)); }
; __device__ __forceinline__ float sigm_f(float x) { return __builtin_amdgcn_rcpf(1.0f + __builtin_amdgcn_exp2f(-1.4426950408889634f * x)); }
; __device__ __forceinline__ float scan16_mul(float x) {
;     ...
;     x *= PG8_DPP_SHR(x, 1); x *= PG8_DPP_SHR(x, 2); x *= PG8_DPP_SHR(x, 4); x *= PG8_DPP_SHR(x, 8);
;     ...
;     return x;
; }
;     __device__ __forceinline__ void operator()(const f32x4 (&acc)[2][2][4][2], const Unit& u, int wr, int wc, int fr, int fq) const {
;     ...
;                     for (int c = 0; c < 8; ++c) {
;                         const float z0 = acc[ai][1][2 * mp][c >> 2][c & 3], z1 = acc[ai][1][2 * mp + 1][c >> 2][c & 3];
;                         const float q0 = acc[ai][0][2 * mp][c >> 2][c & 3], q1 = acc[ai][0][2 * mp + 1][c >> 2][c & 3];
;                         const float s0 = sigm_f(z0), s1 = sigm_f(z1), om = 1.0f - lb[c];
;                         const float e0 = scan16_mul(lb[c] + om * s0);
;                         const float e1 = scan16_mul(lb[c] + om * s1) * bcast15(e0, lane);
;                         const float tt = bcast15(e1, lane);
;                         const float k0 = om * (1.0f - s0) * __builtin_amdgcn_rcpf(e0), k1 = om * (1.0f - s1) * __builtin_amdgcn_rcpf(e1);
;                         qd0[c] = q0 * e0; ki0[c] = k0; ke0[c] = k0 * tt; qd1[c] = q1 * e1; ki1[c] = k1; ke1[c] = k1 * tt; tot[c] = tt;
;                     }
	v_exp_f32_e32 v115, v115
	v_add_f32_e32 v114, 1.0, v114
	v_rcp_f32_e32 v114, v114
	v_mul_f32_e32 v140, v118, v119
	v_add_f32_e32 v115, 1.0, v115
	v_rcp_f32_e32 v180, v115
	v_mov_b32_e32 v115, v137
	v_pk_add_f32 v[118:119], v[114:115], 1.0 op_sel_hi:[1,0] neg_lo:[1,0] neg_hi:[1,0]
	v_fma_f32 v114, v114, v119, v137
	v_mul_f32_e32 v118, v118, v119
	s_nop 0
	v_mul_f32_dpp v114, v114, v114 row_shr:1 row_mask:0xf bank_mask:0xf
	v_mul_f32_e32 v179, v128, v124
	v_mul_f32_e32 v129, v140, v124
	v_mul_f32_dpp v114, v114, v114 row_shr:2 row_mask:0xf bank_mask:0xf
	s_nop 1
	v_mul_f32_dpp v114, v114, v114 row_shr:4 row_mask:0xf bank_mask:0xf
	s_nop 1
	v_mul_f32_dpp v114, v114, v114 row_shr:8 row_mask:0xf bank_mask:0xf
	v_fma_f32 v115, v180, v119, v137
	v_rcp_f32_e32 v181, v114
	v_mul_f32_e32 v121, v121, v114
	v_mul_f32_dpp v115, v115, v115 row_shr:1 row_mask:0xf bank_mask:0xf
	v_mul_f32_e32 v118, v118, v181
	v_sub_f32_e32 v180, 1.0, v180
	v_mul_f32_dpp v115, v115, v115 row_shr:2 row_mask:0xf bank_mask:0xf
	v_mul_f32_e32 v180, v180, v119
	s_nop 0
	v_mul_f32_dpp v115, v115, v115 row_shr:4 row_mask:0xf bank_mask:0xf
	s_nop 1
	v_mul_f32_dpp v115, v115, v115 row_shr:8 row_mask:0xf bank_mask:0xf
	v_mov_b32_e32 v125, 0
	s_nop 0
	v_mul_f32_dpp v115, v114, v115 row_newbcast:15 row_mask:0xf bank_mask:0xf bound_ctrl:1
	v_rcp_f32_e32 v181, v115
	v_mul_f32_e32 v186, v117, v115
	v_mov_b32_dpp v125, v115 row_newbcast:15 row_mask:0xf bank_mask:0xf
	v_pk_add_f32 v[114:115], v[182:183], 1.0 op_sel_hi:[1,0] neg_lo:[1,0] neg_hi:[1,0]
	v_fma_f32 v106, v182, v115, v130
	v_mul_f32_e32 v114, v114, v115
	v_mul_f32_e32 v180, v180, v181
	v_mul_f32_dpp v106, v106, v106 row_shr:1 row_mask:0xf bank_mask:0xf
	v_mul_f32_e32 v181, v118, v125
	v_mul_f32_e32 v117, v180, v125
	v_mul_f32_dpp v106, v106, v106 row_shr:2 row_mask:0xf bank_mask:0xf
	s_nop 1
	v_mul_f32_dpp v106, v106, v106 row_shr:4 row_mask:0xf bank_mask:0xf
	v_mov_b32_e32 v182, 1.0
	s_nop 1
	v_mov_b32_dpp v182, v106 row_shr:8 row_mask:0xf bank_mask:0xf
	v_mul_f32_e32 v182, v106, v182
	v_fma_f32 v106, v110, v115, v130
	v_rcp_f32_e32 v184, v182
	v_sub_f32_e32 v110, 1.0, v110
	v_mul_f32_dpp v106, v106, v106 row_shr:1 row_mask:0xf bank_mask:0xf
	v_mul_f32_e32 v114, v114, v184
	v_mul_f32_e32 v110, v110, v115
	v_mul_f32_dpp v106, v106, v106 row_shr:2 row_mask:0xf bank_mask:0xf
	s_nop 1
	v_mul_f32_dpp v106, v106, v106 row_shr:4 row_mask:0xf bank_mask:0xf
	v_mov_b32_e32 v183, 1.0
	s_nop 1
	v_mov_b32_dpp v183, v106 row_shr:8 row_mask:0xf bank_mask:0xf
	v_mul_f32_e32 v106, v106, v183
	s_nop 1
	v_mul_f32_dpp v183, v182, v106 row_newbcast:15 row_mask:0xf bank_mask:0xf bound_ctrl:1
	v_mul_f32_e32 v188, v98, v183
	v_mul_f32_e32 v98, 0xbfb8aa3b, v111
	v_exp_f32_e32 v98, v98
	v_rcp_f32_e32 v184, v183
	v_mov_b32_e32 v106, 0
	v_add_f32_e32 v98, 1.0, v98
	v_mul_f32_e32 v187, v110, v184
	v_mul_f32_e32 v184, v102, v182
	v_rcp_f32_e32 v182, v98
	v_mov_b32_dpp v106, v183 row_newbcast:15 row_mask:0xf bank_mask:0xf
	v_mul_f32_e32 v98, 0xbfb8aa3b, v107
	v_mov_b32_e32 v183, v131
	v_exp_f32_e32 v98, v98
	v_pk_add_f32 v[110:111], v[182:183], 1.0 op_sel_hi:[1,0] neg_lo:[1,0] neg_hi:[1,0]
	v_fma_f32 v102, v182, v111, v131
	v_add_f32_e32 v98, 1.0, v98
	v_rcp_f32_e32 v98, v98
	v_mul_f32_dpp v102, v102, v102 row_shr:1 row_mask:0xf bank_mask:0xf
	v_mul_f32_e32 v110, v110, v111
	s_nop 0
	v_mul_f32_dpp v102, v102, v102 row_shr:2 row_mask:0xf bank_mask:0xf
	v_mul_f32_e32 v189, v114, v106
	v_mul_f32_e32 v190, v187, v106
	v_mul_f32_dpp v102, v102, v102 row_shr:4 row_mask:0xf bank_mask:0xf
	s_nop 1
	v_mul_f32_dpp v102, v102, v102 row_shr:8 row_mask:0xf bank_mask:0xf
	v_fma_f32 v107, v98, v111, v131
	v_rcp_f32_e32 v183, v102
	v_sub_f32_e32 v98, 1.0, v98
	v_mul_f32_dpp v107, v107, v107 row_shr:1 row_mask:0xf bank_mask:0xf
	v_mul_f32_e32 v110, v110, v183
	v_mul_f32_e32 v98, v98, v111
	v_mul_f32_dpp v107, v107, v107 row_shr:2 row_mask:0xf bank_mask:0xf
	v_mul_f32_e32 v185, v103, v102
	s_nop 0
	v_mul_f32_dpp v107, v107, v107 row_shr:4 row_mask:0xf bank_mask:0xf
	v_mov_b32_e32 v182, 1.0
	s_nop 1
	v_mov_b32_dpp v182, v107 row_shr:8 row_mask:0xf bank_mask:0xf
	v_mul_f32_e32 v107, v107, v182
	s_nop 1
	v_mul_f32_dpp v182, v102, v107 row_newbcast:15 row_mask:0xf bank_mask:0xf bound_ctrl:1
	v_rcp_f32_e32 v183, v182
	v_mul_f32_e32 v203, v99, v182
	v_mul_f32_e32 v99, 0xbfb8aa3b, v108
	v_exp_f32_e32 v99, v99
	v_mul_f32_e32 v191, v98, v183
	v_mul_f32_e32 v98, 0xbfb8aa3b, v112
	v_exp_f32_e32 v98, v98
	v_add_f32_e32 v99, 1.0, v99
	v_rcp_f32_e32 v112, v99
	v_mov_b32_e32 v99, v132
	v_add_f32_e32 v98, 1.0, v98
	v_rcp_f32_e32 v98, v98
	v_mov_b32_e32 v107, 0
	v_pk_add_f32 v[102:103], v[98:99], 1.0 op_sel_hi:[1,0] neg_lo:[1,0] neg_hi:[1,0]
	s_nop 0
	v_fma_f32 v98, v98, v103, v132
	v_mov_b32_dpp v107, v182 row_newbcast:15 row_mask:0xf bank_mask:0xf
	v_mul_f32_e32 v102, v102, v103
	v_mul_f32_dpp v98, v98, v98 row_shr:1 row_mask:0xf bank_mask:0xf
	v_mul_f32_e32 v202, v110, v107
	v_mul_f32_e32 v204, v191, v107
	v_mul_f32_dpp v98, v98, v98 row_shr:2 row_mask:0xf bank_mask:0xf
	s_nop 1
	v_mul_f32_dpp v98, v98, v98 row_shr:4 row_mask:0xf bank_mask:0xf
	s_nop 1
	v_mul_f32_dpp v98, v98, v98 row_shr:8 row_mask:0xf bank_mask:0xf
	v_fma_f32 v99, v112, v103, v132
	v_rcp_f32_e32 v182, v98
	v_mul_f32_e32 v104, v104, v98
	v_mul_f32_dpp v99, v99, v99 row_shr:1 row_mask:0xf bank_mask:0xf
	v_mul_f32_e32 v102, v102, v182
	v_sub_f32_e32 v112, 1.0, v112
	v_mul_f32_dpp v99, v99, v99 row_shr:2 row_mask:0xf bank_mask:0xf
	v_mul_f32_e32 v112, v112, v103
	s_nop 0
	v_mul_f32_dpp v99, v99, v99 row_shr:4 row_mask:0xf bank_mask:0xf
	s_nop 1
	v_mul_f32_dpp v99, v99, v99 row_shr:8 row_mask:0xf bank_mask:0xf
; __device__ __forceinline__ unsigned cvt_pk_bf16(float lo, float hi) { unsigned r; asm volatile("v_cvt_pk_bf16_f32 %0, %1, %2" : "=v"(r) : "v"(lo), "v"(hi)); return r; }
;     __device__ __forceinline__ void operator()(const f32x4 (&acc)[2][2][4][2], const Unit& u, int wr, int wc, int fr, int fq) const {
;     ...
;                     for (int c = 0; c < 8; ++c) {
;                         const float z0 = acc[ai][1][2 * mp][c >> 2][c & 3], z1 = acc[ai][1][2 * mp + 1][c >> 2][c & 3];
;                         const float q0 = acc[ai][0][2 * mp][c >> 2][c & 3], q1 = acc[ai][0][2 * mp + 1][c >> 2][c & 3];
;                         const float s0 = sigm_f(z0), s1 = sigm_f(z1), om = 1.0f - lb[c];
;                         const float e0 = scan16_mul(lb[c] + om * s0);
;                         const float e1 = scan16_mul(lb[c] + om * s1) * bcast15(e0, lane);
;                         const float tt = bcast15(e1, lane);
;                         const float k0 = om * (1.0f - s0) * __builtin_amdgcn_rcpf(e0), k1 = om * (1.0f - s1) * __builtin_amdgcn_rcpf(e1);
;                         qd0[c] = q0 * e0; ki0[c] = k0; ke0[c] = k0 * tt; qd1[c] = q1 * e1; ki1[c] = k1; ke1[c] = k1 * tt; tot[c] = tt;
;                     }
;                     const int rr0 = row0 + ai * HALF + 32 * mp;
;                     const size_t r0 = ((size_t)((rr0 >> 12) * 16 + u.pn) * 4096 + (rr0 & 4095)) * 128 + (wc * 32 + 8 * fq), r1 = r0 + 16 * 128;
;                     u32x4 w;
;                     w.x = cvt_pk_bf16(qd0[0], qd0[1]); w.y = cvt_pk_bf16(qd0[2], qd0[3]); w.z = cvt_pk_bf16(qd0[4], qd0[5]); w.w = cvt_pk_bf16(qd0[6], qd0[7]); *(u32x4*)(QD + r0) = w;
;                     w.x = cvt_pk_bf16(ki0[0], ki0[1]); w.y = cvt_pk_bf16(ki0[2], ki0[3]); w.z = cvt_pk_bf16(ki0[4], ki0[5]); w.w = cvt_pk_bf16(ki0[6], ki0[7]); *(u32x4*)(KI + r0) = w;
;                     w.x = cvt_pk_bf16(ke0[0], ke0[1]); w.y = cvt_pk_bf16(ke0[2], ke0[3]); w.z = cvt_pk_bf16(ke0[4], ke0[5]); w.w = cvt_pk_bf16(ke0[6], ke0[7]); *(u32x4*)(KE + r0) = w;
;                     w.x = cvt_pk_bf16(qd1[0], qd1[1]); w.y = cvt_pk_bf16(qd1[2], qd1[3]); w.z = cvt_pk_bf16(qd1[4], qd1[5]); w.w = cvt_pk_bf16(qd1[6], qd1[7]); *(u32x4*)(QD + r1) = w;
;                     w.x = cvt_pk_bf16(ki1[0], ki1[1]); w.y = cvt_pk_bf16(ki1[2], ki1[3]); w.z = cvt_pk_bf16(ki1[4], ki1[5]); w.w = cvt_pk_bf16(ki1[6], ki1[7]); *(u32x4*)(KI + r1) = w;
	v_mov_b32_e32 v108, 0
	s_nop 0
	v_mul_f32_dpp v99, v98, v99 row_newbcast:15 row_mask:0xf bank_mask:0xf bound_ctrl:1
	v_mul_f32_e32 v98, 0xbfb8aa3b, v113
	v_exp_f32_e32 v98, v98
	v_rcp_f32_e32 v182, v99
	v_mov_b32_e32 v113, v133
	v_mov_b32_dpp v108, v99 row_newbcast:15 row_mask:0xf bank_mask:0xf
	v_add_f32_e32 v98, 1.0, v98
	v_mul_f32_e32 v205, v112, v182
	v_rcp_f32_e32 v112, v98
	v_mul_f32_e32 v98, 0xbfb8aa3b, v109
	v_exp_f32_e32 v98, v98
	v_mul_f32_e32 v206, v100, v99
	v_mul_f32_e32 v207, v102, v108
	v_mul_f32_e32 v208, v205, v108
	v_add_f32_e32 v98, 1.0, v98
	v_rcp_f32_e32 v100, v98
	v_pk_add_f32 v[98:99], v[112:113], 1.0 op_sel_hi:[1,0] neg_lo:[1,0] neg_hi:[1,0]
	v_fma_f32 v109, v112, v99, v133
	v_mul_f32_e32 v98, v98, v99
	s_nop 0
	v_mul_f32_dpp v109, v109, v109 row_shr:1 row_mask:0xf bank_mask:0xf
	s_nop 1
	v_mul_f32_dpp v109, v109, v109 row_shr:2 row_mask:0xf bank_mask:0xf
	s_nop 1
	v_mul_f32_dpp v109, v109, v109 row_shr:4 row_mask:0xf bank_mask:0xf
	v_mov_b32_e32 v112, 1.0
	s_nop 1
	v_mov_b32_dpp v112, v109 row_shr:8 row_mask:0xf bank_mask:0xf
	v_mul_f32_e32 v112, v109, v112
	v_fma_f32 v109, v100, v99, v133
	v_rcp_f32_e32 v182, v112
	v_sub_f32_e32 v100, 1.0, v100
	v_mul_f32_dpp v109, v109, v109 row_shr:1 row_mask:0xf bank_mask:0xf
	v_mul_f32_e32 v98, v98, v182
	v_mul_f32_e32 v100, v100, v99
	v_mul_f32_dpp v109, v109, v109 row_shr:2 row_mask:0xf bank_mask:0xf
	v_mul_f32_e32 v105, v105, v112
	s_nop 0
	v_mul_f32_dpp v109, v109, v109 row_shr:4 row_mask:0xf bank_mask:0xf
	v_mov_b32_e32 v113, 1.0
	s_nop 1
	v_mov_b32_dpp v113, v109 row_shr:8 row_mask:0xf bank_mask:0xf
	v_mul_f32_e32 v109, v109, v113
	s_nop 1
	v_mul_f32_dpp v113, v112, v109 row_newbcast:15 row_mask:0xf bank_mask:0xf bound_ctrl:1
	v_rcp_f32_e32 v182, v113
	v_mov_b32_e32 v109, 0
	v_mul_f32_e32 v209, v100, v182
	s_nop 0
	v_mov_b32_dpp v109, v113 row_newbcast:15 row_mask:0xf bank_mask:0xf
	v_mul_f32_e32 v113, v101, v113
	v_or_b32_e32 v100, v152, v151
	v_mov_b32_e32 v101, s13
	v_lshlrev_b64 v[100:101], 1, v[100:101]
	v_cvt_pk_bf16_f32 v182, v165, v178
	v_cvt_pk_bf16_f32 v183, v120, v121
	v_cvt_pk_bf16_f32 v184, v184, v185
	v_cvt_pk_bf16_f32 v185, v104, v105
	v_lshl_add_u64 v[104:105], s[60:61], 0, v[100:101]
	global_store_dwordx4 v[104:105], v[182:185], off
	v_lshl_add_u64 v[104:105], s[62:63], 0, v[100:101]
	v_mul_f32_e32 v112, v98, v109
	v_cvt_pk_bf16_f32 v182, v164, v174
	v_cvt_pk_bf16_f32 v183, v128, v118
	v_cvt_pk_bf16_f32 v184, v114, v110
	v_cvt_pk_bf16_f32 v185, v102, v98
	global_store_dwordx4 v[104:105], v[182:185], off
	v_lshl_add_u64 v[104:105], s[64:65], 0, v[100:101]
	v_or_b32_e32 v100, 0x1000, v100
	v_cvt_pk_bf16_f32 v182, v173, v177
	v_cvt_pk_bf16_f32 v183, v179, v181
	v_cvt_pk_bf16_f32 v184, v189, v202
	v_cvt_pk_bf16_f32 v185, v207, v112
	global_store_dwordx4 v[104:105], v[182:185], off
	v_lshl_add_u64 v[104:105], s[60:61], 0, v[100:101]
	v_cvt_pk_bf16_f32 v176, v138, v176
	v_cvt_pk_bf16_f32 v177, v116, v186
	v_cvt_pk_bf16_f32 v178, v188, v203
	v_cvt_pk_bf16_f32 v179, v206, v113
	global_store_dwordx4 v[104:105], v[176:179], off
	v_cvt_pk_bf16_f32 v174, v0, v175
	v_cvt_pk_bf16_f32 v175, v140, v180
	v_lshl_add_u64 v[104:105], s[62:63], 0, v[100:101]
	v_lshl_add_u64 v[100:101], s[64:65], 0, v[100:101]
	v_lshlrev_b32_e32 v0, 2, v144
	v_mul_f32_e32 v210, v209, v109
	v_cvt_pk_bf16_f32 v176, v187, v191
	v_cvt_pk_bf16_f32 v177, v205, v209
	global_store_dwordx4 v[104:105], v[174:177], off
	v_cvt_pk_bf16_f32 v172, v172, v126
	v_cvt_pk_bf16_f32 v173, v129, v117
	s_nop 1
	v_cvt_pk_bf16_f32 v174, v190, v204
	v_cvt_pk_bf16_f32 v175, v208, v210
	global_store_dwordx4 v[100:101], v[172:175], off
	s_and_saveexec_b64 s[12:13], s[40:41]
	s_cbranch_execz .LBB0_407
	s_add_u32 s14, s87, s0
	s_addc_u32 s15, s92, s1
	s_lshl_b32 s17, s2, 9
	s_add_u32 s14, s14, s17
	s_addc_u32 s15, s15, 0
	global_store_dwordx4 v0, v[122:125], s[14:15]
	global_store_dwordx4 v0, v[106:109], s[14:15] offset:16
.LBB0_407:
	s_or_b64 exec, exec, s[12:13]
	v_mul_f32_e32 v94, 0xbfb8aa3b, v94
	v_exp_f32_e32 v94, v94
	v_mul_f32_e32 v90, 0xbfb8aa3b, v90
	v_exp_f32_e32 v90, v90
	v_add_f32_e32 v94, 1.0, v94
	v_rcp_f32_e32 v94, v94
	v_add_f32_e32 v90, 1.0, v90
	v_rcp_f32_e32 v98, v90
	v_fma_f32 v90, v94, v139, v134
	v_mul_f32_e32 v95, 0xbfb8aa3b, v95
	v_exp_f32_e32 v95, v95
	v_mul_f32_dpp v90, v90, v90 row_shr:1 row_mask:0xf bank_mask:0xf
	v_sub_f32_e32 v94, 1.0, v94
	v_mul_f32_e32 v91, 0xbfb8aa3b, v91
	v_mul_f32_dpp v90, v90, v90 row_shr:2 row_mask:0xf bank_mask:0xf
	v_mul_f32_e32 v94, v94, v139
	v_add_f32_e32 v95, 1.0, v95
	v_mul_f32_dpp v90, v90, v90 row_shr:4 row_mask:0xf bank_mask:0xf
	v_mov_b32_e32 v100, 1.0
	v_exp_f32_e32 v91, v91
	v_mul_f32_e32 v96, 0xbfb8aa3b, v96
	v_mov_b32_dpp v100, v90 row_shr:8 row_mask:0xf bank_mask:0xf
	v_mul_f32_e32 v100, v90, v100
	v_fma_f32 v90, v98, v139, v134
	v_rcp_f32_e32 v102, v100
	v_sub_f32_e32 v98, 1.0, v98
	v_mul_f32_dpp v90, v90, v90 row_shr:1 row_mask:0xf bank_mask:0xf
	v_mul_f32_e32 v94, v94, v102
	v_mul_f32_e32 v98, v98, v139
	v_mul_f32_dpp v90, v90, v90 row_shr:2 row_mask:0xf bank_mask:0xf
	v_add_f32_e32 v91, 1.0, v91
	v_exp_f32_e32 v96, v96
	v_mul_f32_dpp v90, v90, v90 row_shr:4 row_mask:0xf bank_mask:0xf
	v_mov_b32_e32 v101, 1.0
	v_mul_f32_e32 v92, 0xbfb8aa3b, v92
	v_add_f32_e32 v96, 1.0, v96
	v_mov_b32_dpp v101, v90 row_shr:8 row_mask:0xf bank_mask:0xf
	v_mul_f32_e32 v90, v90, v101
	v_exp_f32_e32 v92, v92
	v_rcp_f32_e32 v96, v96
	v_mul_f32_dpp v101, v100, v90 row_newbcast:15 row_mask:0xf bank_mask:0xf bound_ctrl:1
	v_mov_b32_e32 v90, 0
	v_rcp_f32_e32 v102, v101
	v_mul_f32_e32 v82, v82, v101
	v_mov_b32_dpp v90, v101 row_newbcast:15 row_mask:0xf bank_mask:0xf
; #define PG8_DPP_SHR(v, n) __builtin_bit_cast(float, __builtin_amdgcn_update_dpp(0x3f800000, __builtin_bit_cast(int, v), 0x110 + (n), 0xf, 0xf, false))
; __device__ __forceinline__ float scan16_mul(float x) {
;     ...
;     x *= PG8_DPP_SHR(x, 1); x *= PG8_DPP_SHR(x, 2); x *= PG8_DPP_SHR(x, 4); x *= PG8_DPP_SHR(x, 8);
;     ...
;     return x;
; }
; __device__ __forceinline__ float bcast15(float x, int lane) { (void)lane; return __builtin_bit_cast(float, __builtin_amdgcn_update_dpp(0, __builtin_bit_cast(int, x), 0x15F, 0xf, 0xf, false)); }
; __device__ __forceinline__ float sigm_f(float x) { return __builtin_amdgcn_rcpf(1.0f + __builtin_amdgcn_exp2f(-1.4426950408889634f * x)); }
;     __device__ __forceinline__ void operator()(const f32x4 (&acc)[2][2][4][2], const Unit& u, int wr, int wc, int fr, int fq) const {
;     ...
;                     for (int c = 0; c < 8; ++c) {
;                         const float z0 = acc[ai][1][2 * mp][c >> 2][c & 3], z1 = acc[ai][1][2 * mp + 1][c >> 2][c & 3];
;                         const float q0 = acc[ai][0][2 * mp][c >> 2][c & 3], q1 = acc[ai][0][2 * mp + 1][c >> 2][c & 3];
;                         const float s0 = sigm_f(z0), s1 = sigm_f(z1), om = 1.0f - lb[c];
;                         const float e0 = scan16_mul(lb[c] + om * s0);
;                         const float e1 = scan16_mul(lb[c] + om * s1) * bcast15(e0, lane);
;                         const float tt = bcast15(e1, lane);
;                         const float k0 = om * (1.0f - s0) * __builtin_amdgcn_rcpf(e0), k1 = om * (1.0f - s1) * __builtin_amdgcn_rcpf(e1);
;                         qd0[c] = q0 * e0; ki0[c] = k0; ke0[c] = k0 * tt; qd1[c] = q1 * e1; ki1[c] = k1; ke1[c] = k1 * tt; tot[c] = tt;
;                     }
	v_rcp_f32_e32 v101, v95
	v_mul_f32_e32 v98, v98, v102
	v_rcp_f32_e32 v102, v91
	v_fma_f32 v91, v101, v127, v135
	v_sub_f32_e32 v101, 1.0, v101
	v_mul_f32_e32 v101, v101, v127
	v_mul_f32_dpp v91, v91, v91 row_shr:1 row_mask:0xf bank_mask:0xf
	v_add_f32_e32 v92, 1.0, v92
	s_nop 0
	v_mul_f32_dpp v91, v91, v91 row_shr:2 row_mask:0xf bank_mask:0xf
	v_mul_f32_e32 v97, 0xbfb8aa3b, v97
	s_nop 0
	v_mul_f32_dpp v91, v91, v91 row_shr:4 row_mask:0xf bank_mask:0xf
	v_mov_b32_e32 v95, 1.0
	v_exp_f32_e32 v97, v97
	v_mul_f32_e32 v93, 0xbfb8aa3b, v93
	v_mov_b32_dpp v95, v91 row_shr:8 row_mask:0xf bank_mask:0xf
	v_mul_f32_e32 v104, v91, v95
	v_fma_f32 v91, v102, v127, v135
	v_rcp_f32_e32 v105, v104
	v_sub_f32_e32 v102, 1.0, v102
	v_mul_f32_dpp v91, v91, v91 row_shr:1 row_mask:0xf bank_mask:0xf
	v_mul_f32_e32 v101, v101, v105
	v_mul_f32_e32 v102, v102, v127
	v_mul_f32_dpp v91, v91, v91 row_shr:2 row_mask:0xf bank_mask:0xf
	v_add_f32_e32 v97, 1.0, v97
	v_exp_f32_e32 v93, v93
	v_mul_f32_dpp v91, v91, v91 row_shr:4 row_mask:0xf bank_mask:0xf
	v_add_f32_e32 v93, 1.0, v93
	v_mul_f32_e32 v78, 0xbfb8aa3b, v78
	v_mul_f32_dpp v91, v91, v91 row_shr:8 row_mask:0xf bank_mask:0xf
	v_exp_f32_e32 v78, v78
	v_mul_f32_e32 v74, 0xbfb8aa3b, v74
	v_mul_f32_dpp v106, v104, v91 row_newbcast:15 row_mask:0xf bank_mask:0xf bound_ctrl:1
	v_rcp_f32_e32 v105, v106
	v_mov_b32_e32 v91, 0
	v_add_f32_e32 v78, 1.0, v78
	v_exp_f32_e32 v74, v74
	v_mov_b32_dpp v91, v106 row_newbcast:15 row_mask:0xf bank_mask:0xf
	v_mul_f32_e32 v102, v102, v105
	v_mul_f32_e32 v105, v87, v104
	v_mul_f32_e32 v87, v83, v106
	v_rcp_f32_e32 v106, v92
	v_fma_f32 v92, v96, v141, v136
	v_sub_f32_e32 v96, 1.0, v96
	v_mul_f32_e32 v96, v96, v141
	v_mul_f32_dpp v92, v92, v92 row_shr:1 row_mask:0xf bank_mask:0xf
	v_rcp_f32_e32 v78, v78
	v_add_f32_e32 v74, 1.0, v74
	v_mul_f32_dpp v92, v92, v92 row_shr:2 row_mask:0xf bank_mask:0xf
	s_nop 1
	v_mul_f32_dpp v92, v92, v92 row_shr:4 row_mask:0xf bank_mask:0xf
	v_mov_b32_e32 v107, 1.0
	v_mul_f32_e32 v75, 0xbfb8aa3b, v75
	v_exp_f32_e32 v75, v75
	v_mov_b32_dpp v107, v92 row_shr:8 row_mask:0xf bank_mask:0xf
	v_mul_f32_e32 v107, v92, v107
	v_fma_f32 v92, v106, v141, v136
	v_rcp_f32_e32 v109, v107
	v_sub_f32_e32 v106, 1.0, v106
	v_mul_f32_dpp v92, v92, v92 row_shr:1 row_mask:0xf bank_mask:0xf
	v_mul_f32_e32 v96, v96, v109
	v_mul_f32_e32 v106, v106, v141
	v_mul_f32_dpp v92, v92, v92 row_shr:2 row_mask:0xf bank_mask:0xf
	v_add_f32_e32 v75, 1.0, v75
	s_nop 0
	v_mul_f32_dpp v92, v92, v92 row_shr:4 row_mask:0xf bank_mask:0xf
	v_mov_b32_e32 v108, 1.0
	v_or3_b32 v152, v151, v152, s33
	v_mul_f32_e32 v86, v86, v100
	v_mov_b32_dpp v108, v92 row_shr:8 row_mask:0xf bank_mask:0xf
	v_mul_f32_e32 v92, v92, v108
	v_mul_f32_e32 v88, v88, v107
	v_mul_f32_e32 v100, v94, v90
	v_mul_f32_dpp v108, v107, v92 row_newbcast:15 row_mask:0xf bank_mask:0xf bound_ctrl:1
	v_mov_b32_e32 v92, 0
	v_rcp_f32_e32 v109, v108
	v_mul_f32_e32 v84, v84, v108
	v_mov_b32_dpp v92, v108 row_newbcast:15 row_mask:0xf bank_mask:0xf
	v_rcp_f32_e32 v108, v97
	v_mul_f32_e32 v106, v106, v109
	v_rcp_f32_e32 v109, v93
	v_fma_f32 v93, v108, v119, v137
	v_sub_f32_e32 v108, 1.0, v108
	v_mul_f32_e32 v108, v108, v119
	v_mul_f32_dpp v93, v93, v93 row_shr:1 row_mask:0xf bank_mask:0xf
	v_mul_f32_e32 v104, v101, v91
	v_mul_f32_e32 v107, v96, v92
	v_mul_f32_dpp v93, v93, v93 row_shr:2 row_mask:0xf bank_mask:0xf
	v_mul_f32_e32 v95, v98, v90
	v_mul_f32_e32 v83, v102, v91
	v_mul_f32_dpp v93, v93, v93 row_shr:4 row_mask:0xf bank_mask:0xf
	v_mov_b32_e32 v97, 1.0
	s_nop 1
	v_mov_b32_dpp v97, v93 row_shr:8 row_mask:0xf bank_mask:0xf
	v_mul_f32_e32 v110, v93, v97
	v_fma_f32 v93, v109, v119, v137
	v_rcp_f32_e32 v113, v110
	v_sub_f32_e32 v109, 1.0, v109
	v_mul_f32_dpp v93, v93, v93 row_shr:1 row_mask:0xf bank_mask:0xf
	v_mul_f32_e32 v108, v108, v113
	v_mul_f32_e32 v109, v109, v119
	v_mul_f32_dpp v93, v93, v93 row_shr:2 row_mask:0xf bank_mask:0xf
	s_nop 1
	v_mul_f32_dpp v93, v93, v93 row_shr:4 row_mask:0xf bank_mask:0xf
	s_nop 1
	v_mul_f32_dpp v93, v93, v93 row_shr:8 row_mask:0xf bank_mask:0xf
	v_mul_f32_e32 v97, v106, v92
	s_nop 0
	v_mul_f32_dpp v112, v110, v93 row_newbcast:15 row_mask:0xf bank_mask:0xf bound_ctrl:1
	v_rcp_f32_e32 v113, v112
	v_mov_b32_e32 v93, 0
	v_mul_f32_e32 v109, v109, v113
	s_nop 0
	v_mov_b32_dpp v93, v112 row_newbcast:15 row_mask:0xf bank_mask:0xf
	v_mul_f32_e32 v113, v89, v110
	v_mul_f32_e32 v89, v85, v112
	v_rcp_f32_e32 v112, v74
	v_fma_f32 v74, v78, v115, v130
	v_sub_f32_e32 v78, 1.0, v78
	v_mul_f32_e32 v78, v78, v115
	v_mul_f32_dpp v74, v74, v74 row_shr:1 row_mask:0xf bank_mask:0xf
	v_mul_f32_e32 v110, v108, v93
	v_mul_f32_e32 v85, v109, v93
	v_mul_f32_dpp v74, v74, v74 row_shr:2 row_mask:0xf bank_mask:0xf
	s_nop 1
	v_mul_f32_dpp v74, v74, v74 row_shr:4 row_mask:0xf bank_mask:0xf
	v_mov_b32_e32 v114, 1.0
	s_nop 1
	v_mov_b32_dpp v114, v74 row_shr:8 row_mask:0xf bank_mask:0xf
	v_mul_f32_e32 v114, v74, v114
	v_fma_f32 v74, v112, v115, v130
	v_rcp_f32_e32 v117, v114
	v_mul_f32_e32 v70, v70, v114
	v_mul_f32_dpp v74, v74, v74 row_shr:1 row_mask:0xf bank_mask:0xf
	v_mul_f32_e32 v78, v78, v117
	v_sub_f32_e32 v112, 1.0, v112
	v_mul_f32_dpp v74, v74, v74 row_shr:2 row_mask:0xf bank_mask:0xf
	v_mul_f32_e32 v112, v112, v115
	s_nop 0
	v_mul_f32_dpp v74, v74, v74 row_shr:4 row_mask:0xf bank_mask:0xf
	v_mov_b32_e32 v116, 1.0
	s_nop 1
	v_mov_b32_dpp v116, v74 row_shr:8 row_mask:0xf bank_mask:0xf
	v_mul_f32_e32 v74, v74, v116
	s_nop 1
	v_mul_f32_dpp v116, v114, v74 row_newbcast:15 row_mask:0xf bank_mask:0xf bound_ctrl:1
	v_mul_f32_e32 v114, v66, v116
	v_mul_f32_e32 v66, 0xbfb8aa3b, v79
	v_exp_f32_e32 v66, v66
	v_mov_b32_e32 v74, 0
; __device__ __forceinline__ unsigned cvt_pk_bf16(float lo, float hi) { unsigned r; asm volatile("v_cvt_pk_bf16_f32 %0, %1, %2" : "=v"(r) : "v"(lo), "v"(hi)); return r; }
;     __device__ __forceinline__ void operator()(const f32x4 (&acc)[2][2][4][2], const Unit& u, int wr, int wc, int fr, int fq) const {
;     ...
;                     for (int c = 0; c < 8; ++c) {
;                         const float z0 = acc[ai][1][2 * mp][c >> 2][c & 3], z1 = acc[ai][1][2 * mp + 1][c >> 2][c & 3];
;                         const float q0 = acc[ai][0][2 * mp][c >> 2][c & 3], q1 = acc[ai][0][2 * mp + 1][c >> 2][c & 3];
;                         const float s0 = sigm_f(z0), s1 = sigm_f(z1), om = 1.0f - lb[c];
;                         const float e0 = scan16_mul(lb[c] + om * s0);
;                         const float e1 = scan16_mul(lb[c] + om * s1) * bcast15(e0, lane);
;                         const float tt = bcast15(e1, lane);
;                         const float k0 = om * (1.0f - s0) * __builtin_amdgcn_rcpf(e0), k1 = om * (1.0f - s1) * __builtin_amdgcn_rcpf(e1);
;                         qd0[c] = q0 * e0; ki0[c] = k0; ke0[c] = k0 * tt; qd1[c] = q1 * e1; ki1[c] = k1; ke1[c] = k1 * tt; tot[c] = tt;
;                     }
;                     const int rr0 = row0 + ai * HALF + 32 * mp;
;                     const size_t r0 = ((size_t)((rr0 >> 12) * 16 + u.pn) * 4096 + (rr0 & 4095)) * 128 + (wc * 32 + 8 * fq), r1 = r0 + 16 * 128;
;                     u32x4 w;
;                     w.x = cvt_pk_bf16(qd0[0], qd0[1]); w.y = cvt_pk_bf16(qd0[2], qd0[3]); w.z = cvt_pk_bf16(qd0[4], qd0[5]); w.w = cvt_pk_bf16(qd0[6], qd0[7]); *(u32x4*)(QD + r0) = w;
;                     w.x = cvt_pk_bf16(ki0[0], ki0[1]); w.y = cvt_pk_bf16(ki0[2], ki0[3]); w.z = cvt_pk_bf16(ki0[4], ki0[5]); w.w = cvt_pk_bf16(ki0[6], ki0[7]); *(u32x4*)(KI + r0) = w;
;                     w.x = cvt_pk_bf16(ke0[0], ke0[1]); w.y = cvt_pk_bf16(ke0[2], ke0[3]); w.z = cvt_pk_bf16(ke0[4], ke0[5]); w.w = cvt_pk_bf16(ke0[6], ke0[7]); *(u32x4*)(KE + r0) = w;
;                     w.x = cvt_pk_bf16(qd1[0], qd1[1]); w.y = cvt_pk_bf16(qd1[2], qd1[3]); w.z = cvt_pk_bf16(qd1[4], qd1[5]); w.w = cvt_pk_bf16(qd1[6], qd1[7]); *(u32x4*)(QD + r1) = w;
;                     w.x = cvt_pk_bf16(ki1[0], ki1[1]); w.y = cvt_pk_bf16(ki1[2], ki1[3]); w.z = cvt_pk_bf16(ki1[4], ki1[5]); w.w = cvt_pk_bf16(ki1[6], ki1[7]); *(u32x4*)(KI + r1) = w;
	v_rcp_f32_e32 v117, v116
	v_rcp_f32_e32 v79, v75
	v_add_f32_e32 v66, 1.0, v66
	v_rcp_f32_e32 v66, v66
	v_mov_b32_dpp v74, v116 row_newbcast:15 row_mask:0xf bank_mask:0xf
	v_mul_f32_e32 v112, v112, v117
	v_fma_f32 v75, v66, v111, v131
	v_sub_f32_e32 v66, 1.0, v66
	s_nop 0
	v_mul_f32_dpp v75, v75, v75 row_shr:1 row_mask:0xf bank_mask:0xf
	v_mul_f32_e32 v66, v66, v111
	v_mul_f32_e32 v118, v78, v74
	v_mul_f32_dpp v75, v75, v75 row_shr:2 row_mask:0xf bank_mask:0xf
	v_mul_f32_e32 v120, v112, v74
	s_nop 0
	v_mul_f32_dpp v75, v75, v75 row_shr:4 row_mask:0xf bank_mask:0xf
	v_mov_b32_e32 v116, 1.0
	s_nop 1
	v_mov_b32_dpp v116, v75 row_shr:8 row_mask:0xf bank_mask:0xf
	v_mul_f32_e32 v116, v75, v116
	v_fma_f32 v75, v79, v111, v131
	v_rcp_f32_e32 v121, v116
	v_mul_f32_e32 v71, v71, v116
	v_mul_f32_dpp v75, v75, v75 row_shr:1 row_mask:0xf bank_mask:0xf
	v_mul_f32_e32 v121, v66, v121
	v_sub_f32_e32 v66, 1.0, v79
	v_mul_f32_dpp v75, v75, v75 row_shr:2 row_mask:0xf bank_mask:0xf
	v_mul_f32_e32 v66, v66, v111
	s_nop 0
	v_mul_f32_dpp v75, v75, v75 row_shr:4 row_mask:0xf bank_mask:0xf
	v_mov_b32_e32 v117, 1.0
	s_nop 1
	v_mov_b32_dpp v117, v75 row_shr:8 row_mask:0xf bank_mask:0xf
	v_mul_f32_e32 v75, v75, v117
	s_nop 1
	v_mul_f32_dpp v117, v116, v75 row_newbcast:15 row_mask:0xf bank_mask:0xf bound_ctrl:1
	v_rcp_f32_e32 v79, v117
	v_mov_b32_e32 v75, 0
	v_mul_f32_e32 v79, v66, v79
	v_mul_f32_e32 v66, 0xbfb8aa3b, v80
	v_exp_f32_e32 v66, v66
	v_mov_b32_dpp v75, v117 row_newbcast:15 row_mask:0xf bank_mask:0xf
	v_mul_f32_e32 v117, v67, v117
	v_mul_f32_e32 v67, 0xbfb8aa3b, v76
	v_add_f32_e32 v66, 1.0, v66
	v_rcp_f32_e32 v66, v66
	v_exp_f32_e32 v67, v67
	v_mul_f32_e32 v116, v121, v75
	v_fma_f32 v76, v66, v103, v132
	v_add_f32_e32 v67, 1.0, v67
	v_rcp_f32_e32 v67, v67
	v_mul_f32_dpp v76, v76, v76 row_shr:1 row_mask:0xf bank_mask:0xf
	v_sub_f32_e32 v66, 1.0, v66
	v_mul_f32_e32 v66, v66, v103
	v_mul_f32_dpp v76, v76, v76 row_shr:2 row_mask:0xf bank_mask:0xf
	v_mul_f32_e32 v122, v79, v75
	s_nop 0
	v_mul_f32_dpp v76, v76, v76 row_shr:4 row_mask:0xf bank_mask:0xf
	v_mov_b32_e32 v80, 1.0
	s_nop 1
	v_mov_b32_dpp v80, v76 row_shr:8 row_mask:0xf bank_mask:0xf
	v_mul_f32_e32 v80, v76, v80
	v_fma_f32 v76, v67, v103, v132
	v_rcp_f32_e32 v124, v80
	v_mul_f32_e32 v72, v72, v80
	v_mul_f32_dpp v76, v76, v76 row_shr:1 row_mask:0xf bank_mask:0xf
	v_mul_f32_e32 v124, v66, v124
	v_sub_f32_e32 v66, 1.0, v67
	v_mul_f32_dpp v76, v76, v76 row_shr:2 row_mask:0xf bank_mask:0xf
	v_mul_f32_e32 v66, v66, v103
	s_nop 0
	v_mul_f32_dpp v76, v76, v76 row_shr:4 row_mask:0xf bank_mask:0xf
	v_mov_b32_e32 v123, 1.0
	s_nop 1
	v_mov_b32_dpp v123, v76 row_shr:8 row_mask:0xf bank_mask:0xf
	v_mul_f32_e32 v76, v76, v123
	s_nop 1
	v_mul_f32_dpp v123, v80, v76 row_newbcast:15 row_mask:0xf bank_mask:0xf bound_ctrl:1
	v_rcp_f32_e32 v67, v123
	v_mul_f32_e32 v80, v68, v123
	v_mov_b32_e32 v76, 0
	v_mul_f32_e32 v125, v66, v67
	v_mul_f32_e32 v66, 0xbfb8aa3b, v81
	v_exp_f32_e32 v66, v66
	v_mul_f32_e32 v67, 0xbfb8aa3b, v77
	v_exp_f32_e32 v67, v67
	v_add_f32_e32 v66, 1.0, v66
	v_rcp_f32_e32 v66, v66
	v_add_f32_e32 v67, 1.0, v67
	v_rcp_f32_e32 v67, v67
	v_fma_f32 v68, v66, v99, v133
	v_sub_f32_e32 v66, 1.0, v66
	v_mul_f32_e32 v66, v66, v99
	v_mul_f32_dpp v68, v68, v68 row_shr:1 row_mask:0xf bank_mask:0xf
	v_mov_b32_dpp v76, v123 row_newbcast:15 row_mask:0xf bank_mask:0xf
	v_mul_f32_e32 v123, v124, v76
	v_mul_f32_dpp v68, v68, v68 row_shr:2 row_mask:0xf bank_mask:0xf
	v_mul_f32_e32 v126, v125, v76
	s_nop 0
	v_mul_f32_dpp v68, v68, v68 row_shr:4 row_mask:0xf bank_mask:0xf
	s_nop 1
	v_mul_f32_dpp v68, v68, v68 row_shr:8 row_mask:0xf bank_mask:0xf
	v_fma_f32 v77, v67, v99, v133
	v_rcp_f32_e32 v128, v68
	v_mul_f32_e32 v73, v73, v68
	v_mul_f32_dpp v77, v77, v77 row_shr:1 row_mask:0xf bank_mask:0xf
	v_mul_f32_e32 v128, v66, v128
	v_sub_f32_e32 v66, 1.0, v67
	v_mul_f32_dpp v77, v77, v77 row_shr:2 row_mask:0xf bank_mask:0xf
	v_mul_f32_e32 v66, v66, v99
	s_nop 0
	v_mul_f32_dpp v77, v77, v77 row_shr:4 row_mask:0xf bank_mask:0xf
	v_mov_b32_e32 v81, 1.0
	s_nop 1
	v_mov_b32_dpp v81, v77 row_shr:8 row_mask:0xf bank_mask:0xf
	v_mul_f32_e32 v77, v77, v81
	s_nop 1
	v_mul_f32_dpp v81, v68, v77 row_newbcast:15 row_mask:0xf bank_mask:0xf bound_ctrl:1
	v_rcp_f32_e32 v67, v81
	v_mov_b32_e32 v77, 0
	v_mul_f32_e32 v129, v66, v67
	v_cvt_pk_bf16_f32 v66, v86, v105
	v_cvt_pk_bf16_f32 v67, v88, v113
	v_cvt_pk_bf16_f32 v68, v70, v71
	v_lshlrev_b64 v[70:71], 1, v[152:153]
	v_mov_b32_dpp v77, v81 row_newbcast:15 row_mask:0xf bank_mask:0xf
	v_mul_f32_e32 v81, v69, v81
	v_cvt_pk_bf16_f32 v69, v72, v73
	v_lshl_add_u64 v[72:73], s[60:61], 0, v[70:71]
	global_store_dwordx4 v[72:73], v[66:69], off
	v_lshl_add_u64 v[72:73], s[62:63], 0, v[70:71]
	v_mul_f32_e32 v138, v128, v77
	v_cvt_pk_bf16_f32 v66, v94, v101
	v_cvt_pk_bf16_f32 v67, v96, v108
	v_cvt_pk_bf16_f32 v68, v78, v121
	v_cvt_pk_bf16_f32 v69, v124, v128
	global_store_dwordx4 v[72:73], v[66:69], off
	v_lshl_add_u64 v[72:73], s[64:65], 0, v[70:71]
	v_or_b32_e32 v70, 0x1000, v70
	v_cvt_pk_bf16_f32 v66, v100, v104
	v_cvt_pk_bf16_f32 v67, v107, v110
	v_cvt_pk_bf16_f32 v68, v118, v116
	v_cvt_pk_bf16_f32 v69, v123, v138
	global_store_dwordx4 v[72:73], v[66:69], off
	v_lshl_add_u64 v[72:73], s[60:61], 0, v[70:71]
	v_mul_f32_e32 v140, v129, v77
	v_cvt_pk_bf16_f32 v66, v82, v87
	v_cvt_pk_bf16_f32 v67, v84, v89
	v_cvt_pk_bf16_f32 v68, v114, v117
	v_cvt_pk_bf16_f32 v69, v80, v81
	global_store_dwordx4 v[72:73], v[66:69], off
	v_lshl_add_u64 v[72:73], s[62:63], 0, v[70:71]
	v_lshl_add_u64 v[70:71], s[64:65], 0, v[70:71]
	v_cvt_pk_bf16_f32 v66, v98, v102
	v_cvt_pk_bf16_f32 v67, v106, v109
	v_cvt_pk_bf16_f32 v68, v112, v79
	v_cvt_pk_bf16_f32 v69, v125, v129
	global_store_dwordx4 v[72:73], v[66:69], off
	s_nop 1
	v_cvt_pk_bf16_f32 v66, v95, v83
	v_cvt_pk_bf16_f32 v67, v97, v85
	v_cvt_pk_bf16_f32 v68, v120, v122
	v_cvt_pk_bf16_f32 v69, v126, v140
	global_store_dwordx4 v[70:71], v[66:69], off
	s_and_saveexec_b64 s[12:13], s[40:41]
	s_cbranch_execz .LBB0_409
	s_add_u32 s0, s87, s0
	s_addc_u32 s1, s92, s1
	s_lshl_b32 s2, s2, 9
	s_add_u32 s0, s0, s2
	s_addc_u32 s1, s1, 0
	global_store_dwordx4 v0, v[90:93], s[0:1] offset:512
	global_store_dwordx4 v0, v[74:77], s[0:1] offset:528
; #define PG8_DPP_SHR(v, n) __builtin_bit_cast(float, __builtin_amdgcn_update_dpp(0x3f800000, __builtin_bit_cast(int, v), 0x110 + (n), 0xf, 0xf, false))
; __device__ __forceinline__ float scan16_mul(float x) {
;     ...
;     x *= PG8_DPP_SHR(x, 1); x *= PG8_DPP_SHR(x, 2); x *= PG8_DPP_SHR(x, 4); x *= PG8_DPP_SHR(x, 8);
;     ...
;     return x;
; }
; __device__ __forceinline__ float bcast15(float x, int lane) { (void)lane; return __builtin_bit_cast(float, __builtin_amdgcn_update_dpp(0, __builtin_bit_cast(int, x), 0x15F, 0xf, 0xf, false)); }
; __device__ __forceinline__ float sigm_f(float x) { return __builtin_amdgcn_rcpf(1.0f + __builtin_amdgcn_exp2f(-1.4426950408889634f * x)); }
;     __device__ __forceinline__ void operator()(const f32x4 (&acc)[2][2][4][2], const Unit& u, int wr, int wc, int fr, int fq) const {
;     ...
;                     for (int c = 0; c < 8; ++c) {
;                         const float z0 = acc[ai][1][2 * mp][c >> 2][c & 3], z1 = acc[ai][1][2 * mp + 1][c >> 2][c & 3];
;                         const float q0 = acc[ai][0][2 * mp][c >> 2][c & 3], q1 = acc[ai][0][2 * mp + 1][c >> 2][c & 3];
;                         const float s0 = sigm_f(z0), s1 = sigm_f(z1), om = 1.0f - lb[c];
;                         const float e0 = scan16_mul(lb[c] + om * s0);
;                         const float e1 = scan16_mul(lb[c] + om * s1) * bcast15(e0, lane);
;                         const float tt = bcast15(e1, lane);
;                         const float k0 = om * (1.0f - s0) * __builtin_amdgcn_rcpf(e0), k1 = om * (1.0f - s1) * __builtin_amdgcn_rcpf(e1);
;                         qd0[c] = q0 * e0; ki0[c] = k0; ke0[c] = k0 * tt; qd1[c] = q1 * e1; ki1[c] = k1; ke1[c] = k1 * tt; tot[c] = tt;
;                     }
;                     const int rr0 = row0 + ai * HALF + 32 * mp;
;                     const size_t r0 = ((size_t)((rr0 >> 12) * 16 + u.pn) * 4096 + (rr0 & 4095)) * 128 + (wc * 32 + 8 * fq), r1 = r0 + 16 * 128;
.LBB0_409:
	s_or_b64 exec, exec, s[12:13]
	v_mul_f32_e32 v62, 0xbfb8aa3b, v62
	v_exp_f32_e32 v62, v62
	v_mul_f32_e32 v58, 0xbfb8aa3b, v58
	v_exp_f32_e32 v58, v58
	v_add_f32_e32 v62, 1.0, v62
	v_rcp_f32_e32 v62, v62
	v_add_f32_e32 v58, 1.0, v58
	v_rcp_f32_e32 v69, v58
	v_fma_f32 v58, v62, v139, v134
	v_mul_f32_e32 v63, 0xbfb8aa3b, v63
	v_exp_f32_e32 v63, v63
	v_mul_f32_dpp v58, v58, v58 row_shr:1 row_mask:0xf bank_mask:0xf
	v_mul_f32_e32 v59, 0xbfb8aa3b, v59
	v_exp_f32_e32 v59, v59
	v_mul_f32_dpp v58, v58, v58 row_shr:2 row_mask:0xf bank_mask:0xf
	v_add_f32_e32 v63, 1.0, v63
	v_rcp_f32_e32 v63, v63
	v_mul_f32_dpp v58, v58, v58 row_shr:4 row_mask:0xf bank_mask:0xf
	v_mov_b32_e32 v70, 1.0
	v_add_f32_e32 v59, 1.0, v59
	v_sub_f32_e32 v62, 1.0, v62
	v_mov_b32_dpp v70, v58 row_shr:8 row_mask:0xf bank_mask:0xf
	v_mul_f32_e32 v70, v58, v70
	v_fma_f32 v58, v69, v139, v134
	v_rcp_f32_e32 v72, v70
	v_mul_f32_e32 v54, v54, v70
	v_mul_f32_dpp v58, v58, v58 row_shr:1 row_mask:0xf bank_mask:0xf
	v_mul_f32_e32 v62, v62, v139
	v_mul_f32_e32 v62, v62, v72
	v_mul_f32_dpp v58, v58, v58 row_shr:2 row_mask:0xf bank_mask:0xf
	v_mul_f32_e32 v64, 0xbfb8aa3b, v64
	s_nop 0
	v_mul_f32_dpp v58, v58, v58 row_shr:4 row_mask:0xf bank_mask:0xf
	v_mov_b32_e32 v71, 1.0
	v_exp_f32_e32 v64, v64
	v_mul_f32_e32 v60, 0xbfb8aa3b, v60
	v_mov_b32_dpp v71, v58 row_shr:8 row_mask:0xf bank_mask:0xf
	v_mul_f32_e32 v58, v58, v71
	v_exp_f32_e32 v60, v60
	v_add_f32_e32 v64, 1.0, v64
	v_mul_f32_dpp v71, v70, v58 row_newbcast:15 row_mask:0xf bank_mask:0xf bound_ctrl:1
	v_mov_b32_e32 v58, 0
	v_rcp_f32_e32 v73, v71
	v_mul_f32_e32 v50, v50, v71
	v_mov_b32_dpp v58, v71 row_newbcast:15 row_mask:0xf bank_mask:0xf
	v_rcp_f32_e32 v70, v59
	v_fma_f32 v59, v63, v127, v135
	v_rcp_f32_e32 v64, v64
	v_sub_f32_e32 v63, 1.0, v63
	v_mul_f32_dpp v59, v59, v59 row_shr:1 row_mask:0xf bank_mask:0xf
	v_mul_f32_e32 v63, v63, v127
	v_add_f32_e32 v60, 1.0, v60
	v_mul_f32_dpp v59, v59, v59 row_shr:2 row_mask:0xf bank_mask:0xf
	v_mul_f32_e32 v65, 0xbfb8aa3b, v65
	s_nop 0
	v_mul_f32_dpp v59, v59, v59 row_shr:4 row_mask:0xf bank_mask:0xf
	v_mov_b32_e32 v71, 1.0
	v_exp_f32_e32 v65, v65
	v_mul_f32_e32 v61, 0xbfb8aa3b, v61
	v_mov_b32_dpp v71, v59 row_shr:8 row_mask:0xf bank_mask:0xf
	v_mul_f32_e32 v71, v59, v71
	v_fma_f32 v59, v70, v127, v135
	v_rcp_f32_e32 v75, v71
	v_sub_f32_e32 v70, 1.0, v70
	v_mul_f32_dpp v59, v59, v59 row_shr:1 row_mask:0xf bank_mask:0xf
	v_mul_f32_e32 v70, v70, v127
	v_mul_f32_e32 v63, v63, v75
	v_mul_f32_dpp v59, v59, v59 row_shr:2 row_mask:0xf bank_mask:0xf
	v_rcp_f32_e32 v75, v60
	v_fma_f32 v60, v64, v141, v136
	v_mul_f32_dpp v59, v59, v59 row_shr:4 row_mask:0xf bank_mask:0xf
	v_mov_b32_e32 v72, 1.0
	v_exp_f32_e32 v61, v61
	v_add_f32_e32 v65, 1.0, v65
	v_mov_b32_dpp v72, v59 row_shr:8 row_mask:0xf bank_mask:0xf
	v_mul_f32_e32 v59, v59, v72
	v_rcp_f32_e32 v65, v65
	v_add_f32_e32 v61, 1.0, v61
	v_mul_f32_dpp v72, v71, v59 row_newbcast:15 row_mask:0xf bank_mask:0xf bound_ctrl:1
	v_rcp_f32_e32 v76, v72
	v_sub_f32_e32 v64, 1.0, v64
	v_mul_f32_e32 v64, v64, v141
	v_mul_f32_e32 v46, 0xbfb8aa3b, v46
	v_mul_f32_e32 v70, v70, v76
	v_exp_f32_e32 v46, v46
	v_mul_f32_e32 v42, 0xbfb8aa3b, v42
	v_mul_f32_dpp v60, v60, v60 row_shr:1 row_mask:0xf bank_mask:0xf
	v_exp_f32_e32 v42, v42
	v_add_f32_e32 v46, 1.0, v46
	v_mul_f32_dpp v60, v60, v60 row_shr:2 row_mask:0xf bank_mask:0xf
	v_rcp_f32_e32 v46, v46
	v_add_f32_e32 v42, 1.0, v42
	v_mul_f32_dpp v60, v60, v60 row_shr:4 row_mask:0xf bank_mask:0xf
	v_mov_b32_e32 v76, 1.0
	v_mul_f32_e32 v47, 0xbfb8aa3b, v47
	s_nop 0
	v_mov_b32_dpp v76, v60 row_shr:8 row_mask:0xf bank_mask:0xf
	v_mul_f32_e32 v76, v60, v76
	v_fma_f32 v60, v75, v141, v136
	v_rcp_f32_e32 v78, v76
	v_mul_f32_e32 v56, v56, v76
	v_mul_f32_dpp v60, v60, v60 row_shr:1 row_mask:0xf bank_mask:0xf
	v_mul_f32_e32 v64, v64, v78
	s_nop 0
	v_mul_f32_dpp v60, v60, v60 row_shr:2 row_mask:0xf bank_mask:0xf
	v_exp_f32_e32 v47, v47
	v_add_u32_e32 v68, 0x80, v150
	v_mul_f32_dpp v60, v60, v60 row_shr:4 row_mask:0xf bank_mask:0xf
	v_mov_b32_e32 v77, 1.0
	v_ashrrev_i32_e32 v66, 8, v68
	v_and_b32_e32 v66, -16, v66
	v_mov_b32_dpp v77, v60 row_shr:8 row_mask:0xf bank_mask:0xf
	v_mul_f32_e32 v60, v60, v77
	v_add_u32_e32 v66, s3, v66
	v_ashrrev_i32_e32 v67, 31, v66
	v_mul_f32_dpp v77, v76, v60 row_newbcast:15 row_mask:0xf bank_mask:0xf bound_ctrl:1
	v_mov_b32_e32 v60, 0
	v_rcp_f32_e32 v79, v77
	v_mul_f32_e32 v52, v52, v77
	v_mov_b32_dpp v60, v77 row_newbcast:15 row_mask:0xf bank_mask:0xf
	v_rcp_f32_e32 v76, v61
	v_fma_f32 v61, v65, v119, v137
	v_sub_f32_e32 v65, 1.0, v65
	v_mul_f32_e32 v65, v65, v119
	v_mul_f32_dpp v61, v61, v61 row_shr:1 row_mask:0xf bank_mask:0xf
	v_lshlrev_b64 v[66:67], 19, v[66:67]
	v_lshlrev_b32_e32 v68, 7, v68
	v_mul_f32_dpp v61, v61, v61 row_shr:2 row_mask:0xf bank_mask:0xf
	v_and_b32_e32 v68, 0x7e780, v68
	v_or_b32_e32 v66, v66, v144
	v_mul_f32_dpp v61, v61, v61 row_shr:4 row_mask:0xf bank_mask:0xf
	v_mov_b32_e32 v77, 1.0
	s_addk_i32 s16, 0x80
	s_ashr_i32 s0, s16, 8
	v_mov_b32_dpp v77, v61 row_shr:8 row_mask:0xf bank_mask:0xf
	v_mul_f32_e32 v77, v61, v77
	v_fma_f32 v61, v76, v119, v137
	v_rcp_f32_e32 v81, v77
	v_sub_f32_e32 v76, 1.0, v76
	v_mul_f32_dpp v61, v61, v61 row_shr:1 row_mask:0xf bank_mask:0xf
	v_mul_f32_e32 v76, v76, v119
	v_mul_f32_e32 v65, v65, v81
	v_mul_f32_dpp v61, v61, v61 row_shr:2 row_mask:0xf bank_mask:0xf
	v_rcp_f32_e32 v81, v42
	v_fma_f32 v42, v46, v115, v130
	v_mul_f32_dpp v61, v61, v61 row_shr:4 row_mask:0xf bank_mask:0xf
	v_mov_b32_e32 v78, 1.0
	v_sub_f32_e32 v46, 1.0, v46
	v_mul_f32_e32 v46, v46, v115
	v_mov_b32_dpp v78, v61 row_shr:8 row_mask:0xf bank_mask:0xf
	v_mul_f32_e32 v61, v61, v78
; #define PG8_DPP_SHR(v, n) __builtin_bit_cast(float, __builtin_amdgcn_update_dpp(0x3f800000, __builtin_bit_cast(int, v), 0x110 + (n), 0xf, 0xf, false))
; __device__ __forceinline__ float scan16_mul(float x) {
;     ...
;     x *= PG8_DPP_SHR(x, 1); x *= PG8_DPP_SHR(x, 2); x *= PG8_DPP_SHR(x, 4); x *= PG8_DPP_SHR(x, 8);
;     ...
;     return x;
; }
; __device__ __forceinline__ float bcast15(float x, int lane) { (void)lane; return __builtin_bit_cast(float, __builtin_amdgcn_update_dpp(0, __builtin_bit_cast(int, x), 0x15F, 0xf, 0xf, false)); }
; __device__ __forceinline__ float sigm_f(float x) { return __builtin_amdgcn_rcpf(1.0f + __builtin_amdgcn_exp2f(-1.4426950408889634f * x)); }
;     __device__ __forceinline__ void operator()(const f32x4 (&acc)[2][2][4][2], const Unit& u, int wr, int wc, int fr, int fq) const {
;     ...
;                     for (int c = 0; c < 8; ++c) {
;                         const float z0 = acc[ai][1][2 * mp][c >> 2][c & 3], z1 = acc[ai][1][2 * mp + 1][c >> 2][c & 3];
;                         const float q0 = acc[ai][0][2 * mp][c >> 2][c & 3], q1 = acc[ai][0][2 * mp + 1][c >> 2][c & 3];
;                         const float s0 = sigm_f(z0), s1 = sigm_f(z1), om = 1.0f - lb[c];
;                         const float e0 = scan16_mul(lb[c] + om * s0);
;                         const float e1 = scan16_mul(lb[c] + om * s1) * bcast15(e0, lane);
;                         const float tt = bcast15(e1, lane);
;                         const float k0 = om * (1.0f - s0) * __builtin_amdgcn_rcpf(e0), k1 = om * (1.0f - s1) * __builtin_amdgcn_rcpf(e1);
;                         qd0[c] = q0 * e0; ki0[c] = k0; ke0[c] = k0 * tt; qd1[c] = q1 * e1; ki1[c] = k1; ke1[c] = k1 * tt; tot[c] = tt;
;                     }
	v_sub_f32_e32 v69, 1.0, v69
	v_mov_b32_e32 v59, 0
	v_mul_f32_dpp v78, v77, v61 row_newbcast:15 row_mask:0xf bank_mask:0xf bound_ctrl:1
	v_rcp_f32_e32 v82, v78
	v_mul_f32_e32 v55, v55, v71
	v_sub_f32_e32 v75, 1.0, v75
	v_mov_b32_e32 v61, 0
	v_mul_f32_e32 v76, v76, v82
	v_mul_f32_e32 v57, v57, v77
	s_and_b32 s0, s0, -16
	v_mul_f32_dpp v42, v42, v42 row_shr:1 row_mask:0xf bank_mask:0xf
	v_mul_f32_e32 v69, v69, v139
	v_mov_b32_dpp v59, v72 row_newbcast:15 row_mask:0xf bank_mask:0xf
	v_mul_f32_dpp v42, v42, v42 row_shr:2 row_mask:0xf bank_mask:0xf
	v_mul_f32_e32 v75, v75, v141
	v_mov_b32_dpp v61, v78 row_newbcast:15 row_mask:0xf bank_mask:0xf
	v_mul_f32_dpp v42, v42, v42 row_shr:4 row_mask:0xf bank_mask:0xf
	v_mov_b32_e32 v82, 1.0
	s_add_i32 s0, s0, s3
	v_mul_f32_e32 v69, v69, v73
	v_mov_b32_dpp v82, v42 row_shr:8 row_mask:0xf bank_mask:0xf
	v_mul_f32_e32 v82, v42, v82
	v_fma_f32 v42, v81, v115, v130
	v_rcp_f32_e32 v84, v82
	v_sub_f32_e32 v81, 1.0, v81
	v_mul_f32_dpp v42, v42, v42 row_shr:1 row_mask:0xf bank_mask:0xf
	v_mul_f32_e32 v46, v46, v84
	s_nop 0
	v_mul_f32_dpp v42, v42, v42 row_shr:2 row_mask:0xf bank_mask:0xf
	v_mul_f32_e32 v81, v81, v115
	v_mul_f32_e32 v73, v62, v58
	v_mul_f32_dpp v42, v42, v42 row_shr:4 row_mask:0xf bank_mask:0xf
	v_mov_b32_e32 v83, 1.0
	v_mul_f32_e32 v71, v63, v59
	v_mul_f32_e32 v75, v75, v79
	v_mov_b32_dpp v83, v42 row_shr:8 row_mask:0xf bank_mask:0xf
	v_mul_f32_e32 v42, v42, v83
	v_mul_f32_e32 v79, v64, v60
	v_mul_f32_e32 v77, v65, v61
	v_mul_f32_dpp v83, v82, v42 row_newbcast:15 row_mask:0xf bank_mask:0xf bound_ctrl:1
	v_mul_f32_e32 v82, v38, v82
	v_mul_f32_e32 v38, 0xbfb8aa3b, v43
	v_add_f32_e32 v43, 1.0, v47
	v_exp_f32_e32 v38, v38
	v_rcp_f32_e32 v47, v43
	v_mov_b32_e32 v42, 0
	v_rcp_f32_e32 v85, v83
	s_nop 0
	v_mov_b32_dpp v42, v83 row_newbcast:15 row_mask:0xf bank_mask:0xf
	v_mul_f32_e32 v83, v34, v83
	v_add_f32_e32 v34, 1.0, v38
	v_fma_f32 v38, v47, v111, v131
	v_rcp_f32_e32 v34, v34
	v_sub_f32_e32 v47, 1.0, v47
	v_mul_f32_dpp v38, v38, v38 row_shr:1 row_mask:0xf bank_mask:0xf
	v_mul_f32_e32 v47, v47, v111
	v_mul_f32_e32 v81, v81, v85
	v_mul_f32_dpp v38, v38, v38 row_shr:2 row_mask:0xf bank_mask:0xf
	v_mul_f32_e32 v85, v46, v42
	s_ashr_i32 s1, s0, 31
	v_mul_f32_dpp v38, v38, v38 row_shr:4 row_mask:0xf bank_mask:0xf
	s_lshr_b32 s2, s16, 5
	v_mul_f32_e32 v51, v51, v72
	v_mul_f32_dpp v38, v38, v38 row_shr:8 row_mask:0xf bank_mask:0xf
	v_fma_f32 v43, v34, v111, v131
	v_rcp_f32_e32 v87, v38
	v_sub_f32_e32 v34, 1.0, v34
	v_mul_f32_dpp v43, v43, v43 row_shr:1 row_mask:0xf bank_mask:0xf
	v_mul_f32_e32 v34, v34, v111
	v_mul_f32_e32 v47, v47, v87
	v_mul_f32_dpp v43, v43, v43 row_shr:2 row_mask:0xf bank_mask:0xf
	v_mul_f32_e32 v53, v53, v78
	s_and_b32 s2, s2, 0x7e
	v_mul_f32_dpp v43, v43, v43 row_shr:4 row_mask:0xf bank_mask:0xf
	v_mov_b32_e32 v84, 1.0
	s_lshl_b64 s[0:1], s[0:1], 16
	v_mul_f32_e32 v74, v69, v58
	v_mov_b32_dpp v84, v43 row_shr:8 row_mask:0xf bank_mask:0xf
	v_mul_f32_e32 v43, v43, v84
	v_mul_f32_e32 v72, v70, v59
	v_mul_f32_e32 v80, v75, v60
	v_mul_f32_dpp v84, v38, v43 row_newbcast:15 row_mask:0xf bank_mask:0xf bound_ctrl:1
	v_rcp_f32_e32 v88, v84
	v_mov_b32_e32 v43, 0
	v_mul_f32_e32 v78, v76, v61
	v_mul_f32_e32 v86, v81, v42
	v_mul_f32_e32 v87, v34, v88
	v_mul_f32_e32 v34, 0xbfb8aa3b, v48
	v_exp_f32_e32 v34, v34
	v_mul_f32_e32 v48, v35, v84
	v_mul_f32_e32 v35, 0xbfb8aa3b, v44
	v_exp_f32_e32 v35, v35
	v_add_f32_e32 v34, 1.0, v34
	v_rcp_f32_e32 v34, v34
	v_mul_f32_e32 v88, v39, v38
	v_add_f32_e32 v35, 1.0, v35
	v_fma_f32 v38, v34, v103, v132
	v_rcp_f32_e32 v35, v35
	s_nop 0
	v_mul_f32_dpp v38, v38, v38 row_shr:1 row_mask:0xf bank_mask:0xf
	v_sub_f32_e32 v34, 1.0, v34
	v_mul_f32_e32 v34, v34, v103
	v_mul_f32_dpp v38, v38, v38 row_shr:2 row_mask:0xf bank_mask:0xf
	v_mov_b32_dpp v43, v84 row_newbcast:15 row_mask:0xf bank_mask:0xf
	v_mul_f32_e32 v89, v47, v43
	v_mul_f32_dpp v38, v38, v38 row_shr:4 row_mask:0xf bank_mask:0xf
	v_mul_f32_e32 v84, v87, v43
	s_nop 0
	v_mul_f32_dpp v38, v38, v38 row_shr:8 row_mask:0xf bank_mask:0xf
	v_fma_f32 v39, v35, v103, v132
	v_rcp_f32_e32 v90, v38
	v_mul_f32_e32 v40, v40, v38
	v_mul_f32_dpp v39, v39, v39 row_shr:1 row_mask:0xf bank_mask:0xf
	v_mul_f32_e32 v90, v34, v90
	v_sub_f32_e32 v34, 1.0, v35
	v_mul_f32_dpp v39, v39, v39 row_shr:2 row_mask:0xf bank_mask:0xf
	v_mul_f32_e32 v34, v34, v103
	v_mul_f32_e32 v35, 0xbfb8aa3b, v45
	v_mul_f32_dpp v39, v39, v39 row_shr:4 row_mask:0xf bank_mask:0xf
	v_exp_f32_e32 v35, v35
	v_mov_b32_e32 v45, 0
	v_mul_f32_dpp v39, v39, v39 row_shr:8 row_mask:0xf bank_mask:0xf
	v_add_f32_e32 v35, 1.0, v35
	v_rcp_f32_e32 v35, v35
	v_mul_f32_dpp v39, v38, v39 row_newbcast:15 row_mask:0xf bank_mask:0xf bound_ctrl:1
	v_rcp_f32_e32 v91, v39
	v_mov_b32_e32 v44, 0
	v_mul_f32_e32 v91, v34, v91
	v_mul_f32_e32 v34, 0xbfb8aa3b, v49
	v_exp_f32_e32 v34, v34
	v_mul_f32_e32 v49, v36, v39
	v_mov_b32_dpp v44, v39 row_newbcast:15 row_mask:0xf bank_mask:0xf
	v_add_f32_e32 v34, 1.0, v34
	v_rcp_f32_e32 v34, v34
	v_mul_f32_e32 v92, v90, v44
	v_mul_f32_e32 v93, v91, v44
	v_fma_f32 v36, v34, v99, v133
	v_sub_f32_e32 v34, 1.0, v34
	s_nop 0
	v_mul_f32_dpp v36, v36, v36 row_shr:1 row_mask:0xf bank_mask:0xf
	v_mul_f32_e32 v34, v34, v99
	s_nop 0
	v_mul_f32_dpp v36, v36, v36 row_shr:2 row_mask:0xf bank_mask:0xf
	s_nop 1
	v_mul_f32_dpp v36, v36, v36 row_shr:4 row_mask:0xf bank_mask:0xf
	s_nop 1
	v_mul_f32_dpp v36, v36, v36 row_shr:8 row_mask:0xf bank_mask:0xf
	v_fma_f32 v38, v35, v99, v133
	v_mul_f32_e32 v41, v41, v36
	s_nop 0
	v_mul_f32_dpp v38, v38, v38 row_shr:1 row_mask:0xf bank_mask:0xf
	s_nop 1
	v_mul_f32_dpp v38, v38, v38 row_shr:2 row_mask:0xf bank_mask:0xf
	s_nop 1
; __device__ __forceinline__ unsigned cvt_pk_bf16(float lo, float hi) { unsigned r; asm volatile("v_cvt_pk_bf16_f32 %0, %1, %2" : "=v"(r) : "v"(lo), "v"(hi)); return r; }
;     __device__ __forceinline__ void operator()(const f32x4 (&acc)[2][2][4][2], const Unit& u, int wr, int wc, int fr, int fq) const {
;     ...
;                     for (int c = 0; c < 8; ++c) {
;                         const float z0 = acc[ai][1][2 * mp][c >> 2][c & 3], z1 = acc[ai][1][2 * mp + 1][c >> 2][c & 3];
;                         const float q0 = acc[ai][0][2 * mp][c >> 2][c & 3], q1 = acc[ai][0][2 * mp + 1][c >> 2][c & 3];
;                         const float s0 = sigm_f(z0), s1 = sigm_f(z1), om = 1.0f - lb[c];
;                         const float e0 = scan16_mul(lb[c] + om * s0);
;                         const float e1 = scan16_mul(lb[c] + om * s1) * bcast15(e0, lane);
;                         const float tt = bcast15(e1, lane);
;                         const float k0 = om * (1.0f - s0) * __builtin_amdgcn_rcpf(e0), k1 = om * (1.0f - s1) * __builtin_amdgcn_rcpf(e1);
;                         qd0[c] = q0 * e0; ki0[c] = k0; ke0[c] = k0 * tt; qd1[c] = q1 * e1; ki1[c] = k1; ke1[c] = k1 * tt; tot[c] = tt;
;                     }
;                     const int rr0 = row0 + ai * HALF + 32 * mp;
;                     const size_t r0 = ((size_t)((rr0 >> 12) * 16 + u.pn) * 4096 + (rr0 & 4095)) * 128 + (wc * 32 + 8 * fq), r1 = r0 + 16 * 128;
;                     u32x4 w;
;                     w.x = cvt_pk_bf16(qd0[0], qd0[1]); w.y = cvt_pk_bf16(qd0[2], qd0[3]); w.z = cvt_pk_bf16(qd0[4], qd0[5]); w.w = cvt_pk_bf16(qd0[6], qd0[7]); *(u32x4*)(QD + r0) = w;
;                     w.x = cvt_pk_bf16(ki0[0], ki0[1]); w.y = cvt_pk_bf16(ki0[2], ki0[3]); w.z = cvt_pk_bf16(ki0[4], ki0[5]); w.w = cvt_pk_bf16(ki0[6], ki0[7]); *(u32x4*)(KI + r0) = w;
;                     w.x = cvt_pk_bf16(ke0[0], ke0[1]); w.y = cvt_pk_bf16(ke0[2], ke0[3]); w.z = cvt_pk_bf16(ke0[4], ke0[5]); w.w = cvt_pk_bf16(ke0[6], ke0[7]); *(u32x4*)(KE + r0) = w;
;                     w.x = cvt_pk_bf16(qd1[0], qd1[1]); w.y = cvt_pk_bf16(qd1[2], qd1[3]); w.z = cvt_pk_bf16(qd1[4], qd1[5]); w.w = cvt_pk_bf16(qd1[6], qd1[7]); *(u32x4*)(QD + r1) = w;
;                     w.x = cvt_pk_bf16(ki1[0], ki1[1]); w.y = cvt_pk_bf16(ki1[2], ki1[3]); w.z = cvt_pk_bf16(ki1[4], ki1[5]); w.w = cvt_pk_bf16(ki1[6], ki1[7]); *(u32x4*)(KI + r1) = w;
	v_mul_f32_dpp v38, v38, v38 row_shr:4 row_mask:0xf bank_mask:0xf
	s_nop 1
	v_mul_f32_dpp v38, v38, v38 row_shr:8 row_mask:0xf bank_mask:0xf
	v_rcp_f32_e32 v39, v36
	s_nop 0
	v_mul_f32_dpp v38, v36, v38 row_newbcast:15 row_mask:0xf bank_mask:0xf bound_ctrl:1
	v_rcp_f32_e32 v94, v38
	v_mul_f32_e32 v95, v34, v39
	v_mov_b32_dpp v45, v38 row_newbcast:15 row_mask:0xf bank_mask:0xf
	v_sub_f32_e32 v34, 1.0, v35
	v_mul_f32_e32 v97, v37, v38
	v_or_b32_e32 v38, v66, v68
	v_mov_b32_e32 v39, v67
	v_mul_f32_e32 v34, v34, v99
	v_lshlrev_b64 v[38:39], 1, v[38:39]
	v_mul_f32_e32 v94, v34, v94
	v_cvt_pk_bf16_f32 v34, v54, v55
	v_cvt_pk_bf16_f32 v35, v56, v57
	v_cvt_pk_bf16_f32 v36, v82, v88
	v_cvt_pk_bf16_f32 v37, v40, v41
	v_lshl_add_u64 v[40:41], s[60:61], 0, v[38:39]
	global_store_dwordx4 v[40:41], v[34:37], off
	v_lshl_add_u64 v[40:41], s[62:63], 0, v[38:39]
	v_mul_f32_e32 v96, v95, v45
	v_cvt_pk_bf16_f32 v34, v62, v63
	v_cvt_pk_bf16_f32 v35, v64, v65
	v_cvt_pk_bf16_f32 v36, v46, v47
	v_cvt_pk_bf16_f32 v37, v90, v95
	global_store_dwordx4 v[40:41], v[34:37], off
	v_lshl_add_u64 v[40:41], s[64:65], 0, v[38:39]
	v_or_b32_e32 v38, 0x1000, v38
	v_cvt_pk_bf16_f32 v34, v73, v71
	v_cvt_pk_bf16_f32 v35, v79, v77
	v_cvt_pk_bf16_f32 v36, v85, v89
	v_cvt_pk_bf16_f32 v37, v92, v96
	global_store_dwordx4 v[40:41], v[34:37], off
	v_lshl_add_u64 v[40:41], s[60:61], 0, v[38:39]
	v_mul_f32_e32 v98, v94, v45
	v_cvt_pk_bf16_f32 v34, v50, v51
	v_cvt_pk_bf16_f32 v35, v52, v53
	v_cvt_pk_bf16_f32 v36, v83, v48
	v_cvt_pk_bf16_f32 v37, v49, v97
	global_store_dwordx4 v[40:41], v[34:37], off
	v_lshl_add_u64 v[40:41], s[62:63], 0, v[38:39]
	v_lshl_add_u64 v[38:39], s[64:65], 0, v[38:39]
	v_cvt_pk_bf16_f32 v34, v69, v70
	v_cvt_pk_bf16_f32 v35, v75, v76
	v_cvt_pk_bf16_f32 v36, v81, v87
	v_cvt_pk_bf16_f32 v37, v91, v94
	global_store_dwordx4 v[40:41], v[34:37], off
	s_nop 1
	v_cvt_pk_bf16_f32 v34, v74, v72
	v_cvt_pk_bf16_f32 v35, v80, v78
	v_cvt_pk_bf16_f32 v36, v86, v84
	v_cvt_pk_bf16_f32 v37, v93, v98
	global_store_dwordx4 v[38:39], v[34:37], off
	s_and_saveexec_b64 s[12:13], s[40:41]
	s_cbranch_execz .LBB0_411
	s_add_u32 s3, s87, s0
	s_addc_u32 s15, s92, s1
	s_lshl_b32 s14, s2, 9
	s_add_u32 s14, s3, s14
	s_addc_u32 s15, s15, 0
	global_store_dwordx4 v0, v[58:61], s[14:15]
	global_store_dwordx4 v0, v[42:45], s[14:15] offset:16
.LBB0_411:
	s_or_b64 exec, exec, s[12:13]
	v_mul_f32_e32 v30, 0xbfb8aa3b, v30
	v_exp_f32_e32 v30, v30
	v_mul_f32_e32 v26, 0xbfb8aa3b, v26
	v_exp_f32_e32 v26, v26
	v_add_f32_e32 v30, 1.0, v30
	v_rcp_f32_e32 v30, v30
	v_add_f32_e32 v26, 1.0, v26
	v_rcp_f32_e32 v34, v26
	v_fma_f32 v26, v30, v139, v134
	v_mul_f32_e32 v31, 0xbfb8aa3b, v31
	v_exp_f32_e32 v31, v31
	v_mul_f32_dpp v26, v26, v26 row_shr:1 row_mask:0xf bank_mask:0xf
	v_sub_f32_e32 v30, 1.0, v30
	v_mul_f32_e32 v27, 0xbfb8aa3b, v27
	v_mul_f32_dpp v26, v26, v26 row_shr:2 row_mask:0xf bank_mask:0xf
	v_mul_f32_e32 v30, v30, v139
	v_add_f32_e32 v31, 1.0, v31
	v_mul_f32_dpp v26, v26, v26 row_shr:4 row_mask:0xf bank_mask:0xf
	v_mov_b32_e32 v35, 1.0
	v_exp_f32_e32 v27, v27
	v_mul_f32_e32 v32, 0xbfb8aa3b, v32
	v_mov_b32_dpp v35, v26 row_shr:8 row_mask:0xf bank_mask:0xf
	v_mul_f32_e32 v35, v26, v35
	v_fma_f32 v26, v34, v139, v134
	v_rcp_f32_e32 v37, v35
	v_sub_f32_e32 v34, 1.0, v34
	v_mul_f32_dpp v26, v26, v26 row_shr:1 row_mask:0xf bank_mask:0xf
	v_mul_f32_e32 v30, v30, v37
	v_mul_f32_e32 v34, v34, v139
	v_mul_f32_dpp v26, v26, v26 row_shr:2 row_mask:0xf bank_mask:0xf
	v_add_f32_e32 v27, 1.0, v27
	v_exp_f32_e32 v32, v32
	v_mul_f32_dpp v26, v26, v26 row_shr:4 row_mask:0xf bank_mask:0xf
	v_mov_b32_e32 v36, 1.0
	v_mul_f32_e32 v28, 0xbfb8aa3b, v28
	v_add_f32_e32 v32, 1.0, v32
	v_mov_b32_dpp v36, v26 row_shr:8 row_mask:0xf bank_mask:0xf
	v_mul_f32_e32 v26, v26, v36
	v_exp_f32_e32 v28, v28
	v_rcp_f32_e32 v32, v32
	v_mul_f32_dpp v36, v35, v26 row_newbcast:15 row_mask:0xf bank_mask:0xf bound_ctrl:1
	v_mov_b32_e32 v26, 0
	v_rcp_f32_e32 v37, v36
	v_mul_f32_e32 v18, v18, v36
	v_mov_b32_dpp v26, v36 row_newbcast:15 row_mask:0xf bank_mask:0xf
	v_rcp_f32_e32 v36, v31
	v_mul_f32_e32 v34, v34, v37
	v_rcp_f32_e32 v37, v27
	v_fma_f32 v27, v36, v127, v135
	v_sub_f32_e32 v36, 1.0, v36
	v_mul_f32_e32 v36, v36, v127
	v_mul_f32_dpp v27, v27, v27 row_shr:1 row_mask:0xf bank_mask:0xf
	v_add_f32_e32 v28, 1.0, v28
	s_nop 0
	v_mul_f32_dpp v27, v27, v27 row_shr:2 row_mask:0xf bank_mask:0xf
	v_mul_f32_e32 v33, 0xbfb8aa3b, v33
	s_nop 0
	v_mul_f32_dpp v27, v27, v27 row_shr:4 row_mask:0xf bank_mask:0xf
	v_mov_b32_e32 v31, 1.0
	v_exp_f32_e32 v33, v33
	v_mul_f32_e32 v29, 0xbfb8aa3b, v29
	v_mov_b32_dpp v31, v27 row_shr:8 row_mask:0xf bank_mask:0xf
	v_mul_f32_e32 v38, v27, v31
	v_fma_f32 v27, v37, v127, v135
	v_rcp_f32_e32 v39, v38
	v_sub_f32_e32 v37, 1.0, v37
	v_mul_f32_dpp v27, v27, v27 row_shr:1 row_mask:0xf bank_mask:0xf
	v_mul_f32_e32 v36, v36, v39
	v_mul_f32_e32 v37, v37, v127
	v_mul_f32_dpp v27, v27, v27 row_shr:2 row_mask:0xf bank_mask:0xf
	v_add_f32_e32 v33, 1.0, v33
	v_exp_f32_e32 v29, v29
	v_mul_f32_dpp v27, v27, v27 row_shr:4 row_mask:0xf bank_mask:0xf
	v_add_f32_e32 v29, 1.0, v29
	v_mul_f32_e32 v14, 0xbfb8aa3b, v14
	v_mul_f32_dpp v27, v27, v27 row_shr:8 row_mask:0xf bank_mask:0xf
	v_exp_f32_e32 v14, v14
	v_mul_f32_e32 v10, 0xbfb8aa3b, v10
	v_mul_f32_dpp v40, v38, v27 row_newbcast:15 row_mask:0xf bank_mask:0xf bound_ctrl:1
	v_rcp_f32_e32 v39, v40
	v_mov_b32_e32 v27, 0
	v_add_f32_e32 v14, 1.0, v14
	v_exp_f32_e32 v10, v10
	v_mov_b32_dpp v27, v40 row_newbcast:15 row_mask:0xf bank_mask:0xf
	v_mul_f32_e32 v37, v37, v39
	v_mul_f32_e32 v39, v23, v38
	v_mul_f32_e32 v23, v19, v40
	v_rcp_f32_e32 v40, v28
	v_fma_f32 v28, v32, v141, v136
; #define PG8_DPP_SHR(v, n) __builtin_bit_cast(float, __builtin_amdgcn_update_dpp(0x3f800000, __builtin_bit_cast(int, v), 0x110 + (n), 0xf, 0xf, false))
; __device__ __forceinline__ float scan16_mul(float x) {
;     ...
;     x *= PG8_DPP_SHR(x, 1); x *= PG8_DPP_SHR(x, 2); x *= PG8_DPP_SHR(x, 4); x *= PG8_DPP_SHR(x, 8);
;     ...
;     return x;
; }
; __device__ __forceinline__ float bcast15(float x, int lane) { (void)lane; return __builtin_bit_cast(float, __builtin_amdgcn_update_dpp(0, __builtin_bit_cast(int, x), 0x15F, 0xf, 0xf, false)); }
; __device__ __forceinline__ float sigm_f(float x) { return __builtin_amdgcn_rcpf(1.0f + __builtin_amdgcn_exp2f(-1.4426950408889634f * x)); }
;     __device__ __forceinline__ void operator()(const f32x4 (&acc)[2][2][4][2], const Unit& u, int wr, int wc, int fr, int fq) const {
;     ...
;                     for (int c = 0; c < 8; ++c) {
;                         const float z0 = acc[ai][1][2 * mp][c >> 2][c & 3], z1 = acc[ai][1][2 * mp + 1][c >> 2][c & 3];
;                         const float q0 = acc[ai][0][2 * mp][c >> 2][c & 3], q1 = acc[ai][0][2 * mp + 1][c >> 2][c & 3];
;                         const float s0 = sigm_f(z0), s1 = sigm_f(z1), om = 1.0f - lb[c];
;                         const float e0 = scan16_mul(lb[c] + om * s0);
;                         const float e1 = scan16_mul(lb[c] + om * s1) * bcast15(e0, lane);
;                         const float tt = bcast15(e1, lane);
;                         const float k0 = om * (1.0f - s0) * __builtin_amdgcn_rcpf(e0), k1 = om * (1.0f - s1) * __builtin_amdgcn_rcpf(e1);
;                         qd0[c] = q0 * e0; ki0[c] = k0; ke0[c] = k0 * tt; qd1[c] = q1 * e1; ki1[c] = k1; ke1[c] = k1 * tt; tot[c] = tt;
;                     }
	v_sub_f32_e32 v32, 1.0, v32
	v_mul_f32_e32 v32, v32, v141
	v_mul_f32_dpp v28, v28, v28 row_shr:1 row_mask:0xf bank_mask:0xf
	v_rcp_f32_e32 v14, v14
	v_add_f32_e32 v10, 1.0, v10
	v_mul_f32_dpp v28, v28, v28 row_shr:2 row_mask:0xf bank_mask:0xf
	s_nop 1
	v_mul_f32_dpp v28, v28, v28 row_shr:4 row_mask:0xf bank_mask:0xf
	v_mov_b32_e32 v41, 1.0
	v_mul_f32_e32 v11, 0xbfb8aa3b, v11
	v_exp_f32_e32 v11, v11
	v_mov_b32_dpp v41, v28 row_shr:8 row_mask:0xf bank_mask:0xf
	v_mul_f32_e32 v41, v28, v41
	v_fma_f32 v28, v40, v141, v136
	v_rcp_f32_e32 v43, v41
	v_sub_f32_e32 v40, 1.0, v40
	v_mul_f32_dpp v28, v28, v28 row_shr:1 row_mask:0xf bank_mask:0xf
	v_mul_f32_e32 v32, v32, v43
	v_mul_f32_e32 v40, v40, v141
	v_mul_f32_dpp v28, v28, v28 row_shr:2 row_mask:0xf bank_mask:0xf
	v_add_f32_e32 v11, 1.0, v11
	s_nop 0
	v_mul_f32_dpp v28, v28, v28 row_shr:4 row_mask:0xf bank_mask:0xf
	v_mov_b32_e32 v42, 1.0
	v_or3_b32 v66, v68, v66, s33
	v_mul_f32_e32 v22, v22, v35
	v_mov_b32_dpp v42, v28 row_shr:8 row_mask:0xf bank_mask:0xf
	v_mul_f32_e32 v28, v28, v42
	v_mul_f32_e32 v24, v24, v41
	v_mul_f32_e32 v35, v30, v26
	v_mul_f32_dpp v42, v41, v28 row_newbcast:15 row_mask:0xf bank_mask:0xf bound_ctrl:1
	v_mov_b32_e32 v28, 0
	v_rcp_f32_e32 v43, v42
	v_mul_f32_e32 v20, v20, v42
	v_mov_b32_dpp v28, v42 row_newbcast:15 row_mask:0xf bank_mask:0xf
	v_rcp_f32_e32 v42, v33
	v_mul_f32_e32 v40, v40, v43
	v_rcp_f32_e32 v43, v29
	v_fma_f32 v29, v42, v119, v137
	v_sub_f32_e32 v42, 1.0, v42
	v_fmac_f32_e32 v137, v43, v119
	v_mul_f32_dpp v29, v29, v29 row_shr:1 row_mask:0xf bank_mask:0xf
	v_mul_f32_e32 v42, v42, v119
	v_sub_f32_e32 v43, 1.0, v43
	v_mul_f32_dpp v29, v29, v29 row_shr:2 row_mask:0xf bank_mask:0xf
	v_mul_f32_e32 v43, v43, v119
	v_mul_f32_e32 v38, v36, v27
	v_mul_f32_dpp v29, v29, v29 row_shr:4 row_mask:0xf bank_mask:0xf
	v_mov_b32_e32 v33, 1.0
	v_mul_f32_e32 v41, v32, v28
	v_mul_f32_e32 v31, v34, v26
	v_mov_b32_dpp v33, v29 row_shr:8 row_mask:0xf bank_mask:0xf
	v_mul_f32_e32 v44, v29, v33
	v_mov_b32_e32 v29, 1.0
	v_rcp_f32_e32 v46, v44
	s_nop 0
	v_mov_b32_dpp v29, v137 row_shr:1 row_mask:0xf bank_mask:0xf
	v_mul_f32_e32 v29, v137, v29
	v_mul_f32_e32 v19, v37, v27
	v_mul_f32_e32 v42, v42, v46
	v_mul_f32_dpp v29, v29, v29 row_shr:2 row_mask:0xf bank_mask:0xf
	s_nop 1
	v_mul_f32_dpp v29, v29, v29 row_shr:4 row_mask:0xf bank_mask:0xf
	s_nop 1
	v_mul_f32_dpp v29, v29, v29 row_shr:8 row_mask:0xf bank_mask:0xf
	v_mul_f32_e32 v33, v40, v28
	s_nop 0
	v_mul_f32_dpp v45, v44, v29 row_newbcast:15 row_mask:0xf bank_mask:0xf bound_ctrl:1
	v_rcp_f32_e32 v46, v45
	v_mov_b32_e32 v29, 0
	v_mul_f32_e32 v43, v43, v46
	s_nop 0
	v_mov_b32_dpp v29, v45 row_newbcast:15 row_mask:0xf bank_mask:0xf
	v_mul_f32_e32 v46, v25, v44
	v_mul_f32_e32 v25, v21, v45
	v_rcp_f32_e32 v45, v10
	v_fma_f32 v10, v14, v115, v130
	v_sub_f32_e32 v14, 1.0, v14
	v_mul_f32_e32 v14, v14, v115
	v_mul_f32_dpp v10, v10, v10 row_shr:1 row_mask:0xf bank_mask:0xf
	v_mul_f32_e32 v44, v42, v29
	v_mul_f32_e32 v21, v43, v29
	v_mul_f32_dpp v10, v10, v10 row_shr:2 row_mask:0xf bank_mask:0xf
	s_nop 1
	v_mul_f32_dpp v10, v10, v10 row_shr:4 row_mask:0xf bank_mask:0xf
	v_mov_b32_e32 v47, 1.0
	s_nop 1
	v_mov_b32_dpp v47, v10 row_shr:8 row_mask:0xf bank_mask:0xf
	v_mul_f32_e32 v47, v10, v47
	v_fma_f32 v10, v45, v115, v130
	v_rcp_f32_e32 v49, v47
	v_mul_f32_e32 v6, v6, v47
	v_mul_f32_dpp v10, v10, v10 row_shr:1 row_mask:0xf bank_mask:0xf
	v_mul_f32_e32 v14, v14, v49
	v_sub_f32_e32 v45, 1.0, v45
	v_mul_f32_dpp v10, v10, v10 row_shr:2 row_mask:0xf bank_mask:0xf
	v_mul_f32_e32 v45, v45, v115
	s_nop 0
	v_mul_f32_dpp v10, v10, v10 row_shr:4 row_mask:0xf bank_mask:0xf
	v_mov_b32_e32 v48, 1.0
	s_nop 1
	v_mov_b32_dpp v48, v10 row_shr:8 row_mask:0xf bank_mask:0xf
	v_mul_f32_e32 v10, v10, v48
	s_nop 1
	v_mul_f32_dpp v48, v47, v10 row_newbcast:15 row_mask:0xf bank_mask:0xf bound_ctrl:1
	v_mul_f32_e32 v47, v2, v48
	v_mul_f32_e32 v2, 0xbfb8aa3b, v15
	v_exp_f32_e32 v2, v2
	v_mov_b32_e32 v10, 0
	v_rcp_f32_e32 v49, v48
	v_rcp_f32_e32 v15, v11
	v_add_f32_e32 v2, 1.0, v2
	v_rcp_f32_e32 v2, v2
	v_mov_b32_dpp v10, v48 row_newbcast:15 row_mask:0xf bank_mask:0xf
	v_mul_f32_e32 v45, v45, v49
	v_fma_f32 v11, v2, v111, v131
	v_sub_f32_e32 v2, 1.0, v2
	s_nop 0
	v_mul_f32_dpp v11, v11, v11 row_shr:1 row_mask:0xf bank_mask:0xf
	v_mul_f32_e32 v2, v2, v111
	v_mul_f32_e32 v50, v14, v10
	v_mul_f32_dpp v11, v11, v11 row_shr:2 row_mask:0xf bank_mask:0xf
	v_mul_f32_e32 v51, v45, v10
	s_nop 0
	v_mul_f32_dpp v11, v11, v11 row_shr:4 row_mask:0xf bank_mask:0xf
	v_mov_b32_e32 v48, 1.0
	s_nop 1
	v_mov_b32_dpp v48, v11 row_shr:8 row_mask:0xf bank_mask:0xf
	v_mul_f32_e32 v48, v11, v48
	v_fma_f32 v11, v15, v111, v131
	v_rcp_f32_e32 v52, v48
	v_mul_f32_e32 v7, v7, v48
	v_mul_f32_dpp v11, v11, v11 row_shr:1 row_mask:0xf bank_mask:0xf
	v_mul_f32_e32 v52, v2, v52
	v_sub_f32_e32 v2, 1.0, v15
	v_mul_f32_dpp v11, v11, v11 row_shr:2 row_mask:0xf bank_mask:0xf
	v_mul_f32_e32 v2, v2, v111
	s_nop 0
	v_mul_f32_dpp v11, v11, v11 row_shr:4 row_mask:0xf bank_mask:0xf
; __device__ __forceinline__ unsigned cvt_pk_bf16(float lo, float hi) { unsigned r; asm volatile("v_cvt_pk_bf16_f32 %0, %1, %2" : "=v"(r) : "v"(lo), "v"(hi)); return r; }
;     __device__ __forceinline__ void operator()(const f32x4 (&acc)[2][2][4][2], const Unit& u, int wr, int wc, int fr, int fq) const {
;     ...
;                     for (int c = 0; c < 8; ++c) {
;                         const float z0 = acc[ai][1][2 * mp][c >> 2][c & 3], z1 = acc[ai][1][2 * mp + 1][c >> 2][c & 3];
;                         const float q0 = acc[ai][0][2 * mp][c >> 2][c & 3], q1 = acc[ai][0][2 * mp + 1][c >> 2][c & 3];
;                         const float s0 = sigm_f(z0), s1 = sigm_f(z1), om = 1.0f - lb[c];
;                         const float e0 = scan16_mul(lb[c] + om * s0);
;                         const float e1 = scan16_mul(lb[c] + om * s1) * bcast15(e0, lane);
;                         const float tt = bcast15(e1, lane);
;                         const float k0 = om * (1.0f - s0) * __builtin_amdgcn_rcpf(e0), k1 = om * (1.0f - s1) * __builtin_amdgcn_rcpf(e1);
;                         qd0[c] = q0 * e0; ki0[c] = k0; ke0[c] = k0 * tt; qd1[c] = q1 * e1; ki1[c] = k1; ke1[c] = k1 * tt; tot[c] = tt;
;                     }
;                     const int rr0 = row0 + ai * HALF + 32 * mp;
;                     const size_t r0 = ((size_t)((rr0 >> 12) * 16 + u.pn) * 4096 + (rr0 & 4095)) * 128 + (wc * 32 + 8 * fq), r1 = r0 + 16 * 128;
;                     u32x4 w;
;                     w.x = cvt_pk_bf16(qd0[0], qd0[1]); w.y = cvt_pk_bf16(qd0[2], qd0[3]); w.z = cvt_pk_bf16(qd0[4], qd0[5]); w.w = cvt_pk_bf16(qd0[6], qd0[7]); *(u32x4*)(QD + r0) = w;
;                     w.x = cvt_pk_bf16(ki0[0], ki0[1]); w.y = cvt_pk_bf16(ki0[2], ki0[3]); w.z = cvt_pk_bf16(ki0[4], ki0[5]); w.w = cvt_pk_bf16(ki0[6], ki0[7]); *(u32x4*)(KI + r0) = w;
;                     w.x = cvt_pk_bf16(ke0[0], ke0[1]); w.y = cvt_pk_bf16(ke0[2], ke0[3]); w.z = cvt_pk_bf16(ke0[4], ke0[5]); w.w = cvt_pk_bf16(ke0[6], ke0[7]); *(u32x4*)(KE + r0) = w;
;                     w.x = cvt_pk_bf16(qd1[0], qd1[1]); w.y = cvt_pk_bf16(qd1[2], qd1[3]); w.z = cvt_pk_bf16(qd1[4], qd1[5]); w.w = cvt_pk_bf16(qd1[6], qd1[7]); *(u32x4*)(QD + r1) = w;
;                     w.x = cvt_pk_bf16(ki1[0], ki1[1]); w.y = cvt_pk_bf16(ki1[2], ki1[3]); w.z = cvt_pk_bf16(ki1[4], ki1[5]); w.w = cvt_pk_bf16(ki1[6], ki1[7]); *(u32x4*)(KI + r1) = w;
	v_mov_b32_e32 v49, 1.0
	s_nop 1
	v_mov_b32_dpp v49, v11 row_shr:8 row_mask:0xf bank_mask:0xf
	v_mul_f32_e32 v11, v11, v49
	s_nop 1
	v_mul_f32_dpp v49, v48, v11 row_newbcast:15 row_mask:0xf bank_mask:0xf bound_ctrl:1
	v_rcp_f32_e32 v15, v49
	v_mov_b32_e32 v11, 0
	v_mul_f32_e32 v15, v2, v15
	v_mul_f32_e32 v2, 0xbfb8aa3b, v16
	v_exp_f32_e32 v2, v2
	v_mov_b32_dpp v11, v49 row_newbcast:15 row_mask:0xf bank_mask:0xf
	v_mul_f32_e32 v49, v3, v49
	v_mul_f32_e32 v3, 0xbfb8aa3b, v12
	v_add_f32_e32 v2, 1.0, v2
	v_rcp_f32_e32 v2, v2
	v_exp_f32_e32 v3, v3
	v_mul_f32_e32 v48, v52, v11
	v_fma_f32 v12, v2, v103, v132
	v_add_f32_e32 v3, 1.0, v3
	v_rcp_f32_e32 v3, v3
	v_mul_f32_dpp v12, v12, v12 row_shr:1 row_mask:0xf bank_mask:0xf
	v_sub_f32_e32 v2, 1.0, v2
	v_mul_f32_e32 v2, v2, v103
	v_mul_f32_dpp v12, v12, v12 row_shr:2 row_mask:0xf bank_mask:0xf
	v_mul_f32_e32 v53, v15, v11
	s_nop 0
	v_mul_f32_dpp v12, v12, v12 row_shr:4 row_mask:0xf bank_mask:0xf
	v_mov_b32_e32 v16, 1.0
	s_nop 1
	v_mov_b32_dpp v16, v12 row_shr:8 row_mask:0xf bank_mask:0xf
	v_mul_f32_e32 v16, v12, v16
	v_fma_f32 v12, v3, v103, v132
	v_rcp_f32_e32 v55, v16
	v_mul_f32_e32 v8, v8, v16
	v_mul_f32_dpp v12, v12, v12 row_shr:1 row_mask:0xf bank_mask:0xf
	v_mul_f32_e32 v55, v2, v55
	v_sub_f32_e32 v2, 1.0, v3
	v_mul_f32_dpp v12, v12, v12 row_shr:2 row_mask:0xf bank_mask:0xf
	v_mul_f32_e32 v2, v2, v103
	s_nop 0
	v_mul_f32_dpp v12, v12, v12 row_shr:4 row_mask:0xf bank_mask:0xf
	v_mov_b32_e32 v54, 1.0
	s_nop 1
	v_mov_b32_dpp v54, v12 row_shr:8 row_mask:0xf bank_mask:0xf
	v_mul_f32_e32 v12, v12, v54
	s_nop 1
	v_mul_f32_dpp v54, v16, v12 row_newbcast:15 row_mask:0xf bank_mask:0xf bound_ctrl:1
	v_rcp_f32_e32 v3, v54
	v_mul_f32_e32 v16, v4, v54
	v_mov_b32_e32 v12, 0
	v_mul_f32_e32 v56, v2, v3
	v_mul_f32_e32 v2, 0xbfb8aa3b, v17
	v_exp_f32_e32 v2, v2
	v_mul_f32_e32 v3, 0xbfb8aa3b, v13
	v_exp_f32_e32 v3, v3
	v_add_f32_e32 v2, 1.0, v2
	v_rcp_f32_e32 v2, v2
	v_add_f32_e32 v3, 1.0, v3
	v_rcp_f32_e32 v3, v3
	v_fma_f32 v4, v2, v99, v133
	v_sub_f32_e32 v2, 1.0, v2
	v_fmac_f32_e32 v133, v3, v99
	v_mul_f32_dpp v4, v4, v4 row_shr:1 row_mask:0xf bank_mask:0xf
	v_mul_f32_e32 v2, v2, v99
	v_mov_b32_dpp v12, v54 row_newbcast:15 row_mask:0xf bank_mask:0xf
	v_mul_f32_dpp v4, v4, v4 row_shr:2 row_mask:0xf bank_mask:0xf
	v_mul_f32_e32 v54, v55, v12
	v_mul_f32_e32 v57, v56, v12
	v_mul_f32_dpp v4, v4, v4 row_shr:4 row_mask:0xf bank_mask:0xf
	s_nop 1
	v_mul_f32_dpp v4, v4, v4 row_shr:8 row_mask:0xf bank_mask:0xf
	v_mov_b32_e32 v13, 1.0
	v_rcp_f32_e32 v58, v4
	v_mul_f32_e32 v9, v9, v4
	v_mov_b32_dpp v13, v133 row_shr:1 row_mask:0xf bank_mask:0xf
	v_mul_f32_e32 v13, v133, v13
	v_mul_f32_e32 v58, v2, v58
	v_sub_f32_e32 v2, 1.0, v3
	v_mul_f32_dpp v13, v13, v13 row_shr:2 row_mask:0xf bank_mask:0xf
	v_mul_f32_e32 v2, v2, v99
	s_nop 0
	v_mul_f32_dpp v13, v13, v13 row_shr:4 row_mask:0xf bank_mask:0xf
	v_mov_b32_e32 v17, 1.0
	s_nop 1
	v_mov_b32_dpp v17, v13 row_shr:8 row_mask:0xf bank_mask:0xf
	v_mul_f32_e32 v13, v13, v17
	s_nop 1
	v_mul_f32_dpp v17, v4, v13 row_newbcast:15 row_mask:0xf bank_mask:0xf bound_ctrl:1
	v_rcp_f32_e32 v3, v17
	v_mov_b32_e32 v13, 0
	v_mul_f32_e32 v59, v2, v3
	v_cvt_pk_bf16_f32 v2, v22, v39
	v_cvt_pk_bf16_f32 v3, v24, v46
	v_cvt_pk_bf16_f32 v4, v6, v7
	v_lshlrev_b64 v[6:7], 1, v[66:67]
	v_mov_b32_dpp v13, v17 row_newbcast:15 row_mask:0xf bank_mask:0xf
	v_mul_f32_e32 v17, v5, v17
	v_cvt_pk_bf16_f32 v5, v8, v9
	v_lshl_add_u64 v[8:9], s[60:61], 0, v[6:7]
	global_store_dwordx4 v[8:9], v[2:5], off
	v_lshl_add_u64 v[8:9], s[62:63], 0, v[6:7]
	v_mul_f32_e32 v60, v58, v13
	v_cvt_pk_bf16_f32 v2, v30, v36
	v_cvt_pk_bf16_f32 v3, v32, v42
	v_cvt_pk_bf16_f32 v4, v14, v52
	v_cvt_pk_bf16_f32 v5, v55, v58
	global_store_dwordx4 v[8:9], v[2:5], off
	v_lshl_add_u64 v[8:9], s[64:65], 0, v[6:7]
	v_or_b32_e32 v6, 0x1000, v6
	v_cvt_pk_bf16_f32 v2, v35, v38
	v_cvt_pk_bf16_f32 v3, v41, v44
	v_cvt_pk_bf16_f32 v4, v50, v48
	v_cvt_pk_bf16_f32 v5, v54, v60
	global_store_dwordx4 v[8:9], v[2:5], off
	v_lshl_add_u64 v[8:9], s[60:61], 0, v[6:7]
	v_mul_f32_e32 v61, v59, v13
	v_cvt_pk_bf16_f32 v2, v18, v23
	v_cvt_pk_bf16_f32 v3, v20, v25
	v_cvt_pk_bf16_f32 v4, v47, v49
	v_cvt_pk_bf16_f32 v5, v16, v17
	global_store_dwordx4 v[8:9], v[2:5], off
	v_lshl_add_u64 v[8:9], s[62:63], 0, v[6:7]
	v_lshl_add_u64 v[6:7], s[64:65], 0, v[6:7]
	v_cvt_pk_bf16_f32 v2, v34, v37
	v_cvt_pk_bf16_f32 v3, v40, v43
	v_cvt_pk_bf16_f32 v4, v45, v15
	v_cvt_pk_bf16_f32 v5, v56, v59
	global_store_dwordx4 v[8:9], v[2:5], off
	s_nop 1
	v_cvt_pk_bf16_f32 v2, v31, v19
	v_cvt_pk_bf16_f32 v3, v33, v21
	v_cvt_pk_bf16_f32 v4, v51, v53
	v_cvt_pk_bf16_f32 v5, v57, v61
	global_store_dwordx4 v[6:7], v[2:5], off
	s_and_saveexec_b64 s[12:13], s[40:41]
	s_cbranch_execz .LBB0_413
	s_add_u32 s0, s87, s0
	s_addc_u32 s1, s92, s1
	s_lshl_b32 s2, s2, 9
	s_add_u32 s0, s0, s2
	s_addc_u32 s1, s1, 0
	global_store_dwordx4 v0, v[26:29], s[0:1] offset:512
	global_store_dwordx4 v0, v[10:13], s[0:1] offset:528
